# GEMM K loops: first K iteration peeled with inline-zero C operands instead of zeroing 128 accumulator registers per tile (8 loops), on top of v44
# speedup vs baseline: 1.0093x; 1.0080x over previous
.LBB0_338:
	s_add_u32 s79, s26, 0x100
	s_addc_u32 s80, s27, 0
	s_add_u32 s24, s24, 0x80080
	s_addc_u32 s25, s25, 0
	s_mov_b32 s81, -2
	s_add_u32 s26, s24, 0xfff80080
	s_addc_u32 s27, s25, -1
	s_add_i32 s82, 0, 0x10000
	s_cmp_eq_u32 s81, 28
	s_cselect_b32 s27, s21, s27
	s_cselect_b32 s26, s20, s26
	v_add_u32_e32 v96, s82, v141
	s_cselect_b32 s29, s23, s80
	s_cselect_b32 s28, s22, s79
	s_add_i32 s84, 0, 0x14000
	ds_read_b128 v[144:147], v96
	ds_read_b128 v[148:151], v96 offset:1024
	ds_read_b128 v[152:155], v96 offset:2048
	ds_read_b128 v[156:159], v96 offset:3072
	v_add_u32_e32 v96, s84, v141
	ds_read_b128 v[160:163], v96
	ds_read_b128 v[164:167], v96 offset:1024
	ds_read_b128 v[168:171], v96 offset:2048
	ds_read_b128 v[172:175], v96 offset:3072
	v_mov_b32_e32 v96, v136
	ds_read_b128 v[176:179], v142
	ds_read_b128 v[180:183], v142 offset:1024
	ds_read_b128 v[184:187], v142 offset:2048
	ds_read_b128 v[188:191], v142 offset:3072
	ds_read_b128 v[192:195], v142 offset:4096
	ds_read_b128 v[196:199], v142 offset:5120
	ds_read_b128 v[200:203], v142 offset:6144
	ds_read_b128 v[222:225], v142 offset:7168
	s_add_i32 m0, s36, 0xc000
	s_nop 0
	global_load_lds_dwordx4 v96, s[24:25]
	v_mov_b32_e32 v96, v138
	s_add_i32 m0, s36, 0xe000
	s_nop 0
	global_load_lds_dwordx4 v96, s[24:25]
	s_waitcnt vmcnt(8)
	s_waitcnt lgkmcnt(0)
	s_barrier
	s_setprio 1
	s_waitcnt lgkmcnt(0)
	v_mfma_f32_16x16x32_bf16 v[126:129], v[144:147], v[176:179], 0
	v_mfma_f32_16x16x32_bf16 v[122:125], v[152:155], v[176:179], 0
	v_mfma_f32_16x16x32_bf16 v[118:121], v[144:147], v[184:187], 0
	v_mfma_f32_16x16x32_bf16 v[114:117], v[152:155], v[184:187], 0
	v_mfma_f32_16x16x32_bf16 v[102:105], v[144:147], v[192:195], 0
	v_mfma_f32_16x16x32_bf16 v[98:101], v[152:155], v[192:195], 0
	v_mfma_f32_16x16x32_bf16 v[84:87], v[144:147], v[200:203], 0
	v_mfma_f32_16x16x32_bf16 v[80:83], v[152:155], v[200:203], 0
	v_mfma_f32_16x16x32_bf16 v[126:129], v[148:151], v[180:183], v[126:129]
	v_mfma_f32_16x16x32_bf16 v[122:125], v[156:159], v[180:183], v[122:125]
	v_mfma_f32_16x16x32_bf16 v[118:121], v[148:151], v[188:191], v[118:121]
	v_mfma_f32_16x16x32_bf16 v[114:117], v[156:159], v[188:191], v[114:117]
	v_mfma_f32_16x16x32_bf16 v[102:105], v[148:151], v[196:199], v[102:105]
	v_mfma_f32_16x16x32_bf16 v[98:101], v[156:159], v[196:199], v[98:101]
	v_mfma_f32_16x16x32_bf16 v[84:87], v[148:151], v[222:225], v[84:87]
	v_mfma_f32_16x16x32_bf16 v[80:83], v[156:159], v[222:225], v[80:83]
	s_setprio 0
	s_setprio 1
	v_mfma_f32_16x16x32_bf16 v[110:113], v[160:163], v[176:179], 0
	v_mfma_f32_16x16x32_bf16 v[106:109], v[168:171], v[176:179], 0
	v_mfma_f32_16x16x32_bf16 v[92:95], v[160:163], v[184:187], 0
	v_mfma_f32_16x16x32_bf16 v[88:91], v[168:171], v[184:187], 0
	v_mfma_f32_16x16x32_bf16 v[76:79], v[160:163], v[192:195], 0
	v_mfma_f32_16x16x32_bf16 v[72:75], v[168:171], v[192:195], 0
	v_mfma_f32_16x16x32_bf16 v[68:71], v[160:163], v[200:203], 0
	v_mfma_f32_16x16x32_bf16 v[64:67], v[168:171], v[200:203], 0
	v_mfma_f32_16x16x32_bf16 v[110:113], v[164:167], v[180:183], v[110:113]
	v_mfma_f32_16x16x32_bf16 v[106:109], v[172:175], v[180:183], v[106:109]
	v_mfma_f32_16x16x32_bf16 v[92:95], v[164:167], v[188:191], v[92:95]
	v_mfma_f32_16x16x32_bf16 v[88:91], v[172:175], v[188:191], v[88:91]
	v_mfma_f32_16x16x32_bf16 v[76:79], v[164:167], v[196:199], v[76:79]
	v_mfma_f32_16x16x32_bf16 v[72:75], v[172:175], v[196:199], v[72:75]
	v_mfma_f32_16x16x32_bf16 v[68:71], v[164:167], v[222:225], v[68:71]
	v_mfma_f32_16x16x32_bf16 v[64:67], v[172:175], v[222:225], v[64:67]
	s_setprio 0
	s_barrier
	v_mov_b32_e32 v96, v137
	s_add_i32 s82, s82, s35
	ds_read_b128 v[176:179], v142 offset:16384
	ds_read_b128 v[180:183], v142 offset:17408
	ds_read_b128 v[184:187], v142 offset:18432
	ds_read_b128 v[188:191], v142 offset:19456
	ds_read_b128 v[192:195], v142 offset:20480
	ds_read_b128 v[196:199], v142 offset:21504
	ds_read_b128 v[200:203], v142 offset:22528
	ds_read_b128 v[222:225], v142 offset:23552
	s_mov_b32 m0, s82
	s_nop 0
	global_load_lds_dwordx4 v96, s[28:29]
	v_mov_b32_e32 v96, v139
	s_add_i32 m0, s82, 0x2000
	s_add_u32 s82, s28, 0x80000
	global_load_lds_dwordx4 v96, s[28:29]
	s_addc_u32 s83, s29, 0
	v_mov_b32_e32 v96, v137
	s_add_i32 s84, s84, s35
	s_mov_b32 m0, s84
	s_nop 0
	global_load_lds_dwordx4 v96, s[82:83]
	v_mov_b32_e32 v96, v139
	s_add_i32 m0, s84, 0x2000
	s_nop 0
	global_load_lds_dwordx4 v96, s[82:83]
	v_mov_b32_e32 v96, v136
	s_mov_b32 m0, s36
	s_nop 0
	global_load_lds_dwordx4 v96, s[26:27]
	v_mov_b32_e32 v96, v138
	s_mov_b32 m0, s37
	s_nop 0
	global_load_lds_dwordx4 v96, s[26:27]
	s_waitcnt vmcnt(8)
	s_waitcnt lgkmcnt(0)
	s_barrier
	s_setprio 1
	s_waitcnt lgkmcnt(0)
	v_mfma_f32_16x16x32_bf16 v[60:63], v[144:147], v[176:179], 0
	v_mfma_f32_16x16x32_bf16 v[56:59], v[152:155], v[176:179], 0
	v_mfma_f32_16x16x32_bf16 v[52:55], v[144:147], v[184:187], 0
	v_mfma_f32_16x16x32_bf16 v[48:51], v[152:155], v[184:187], 0
	v_mfma_f32_16x16x32_bf16 v[36:39], v[144:147], v[192:195], 0
	v_mfma_f32_16x16x32_bf16 v[32:35], v[152:155], v[192:195], 0
	v_mfma_f32_16x16x32_bf16 v[20:23], v[144:147], v[200:203], 0
	v_mfma_f32_16x16x32_bf16 v[16:19], v[152:155], v[200:203], 0
	v_mfma_f32_16x16x32_bf16 v[60:63], v[148:151], v[180:183], v[60:63]
	v_mfma_f32_16x16x32_bf16 v[56:59], v[156:159], v[180:183], v[56:59]
	v_mfma_f32_16x16x32_bf16 v[52:55], v[148:151], v[188:191], v[52:55]
	v_mfma_f32_16x16x32_bf16 v[48:51], v[156:159], v[188:191], v[48:51]
	v_mfma_f32_16x16x32_bf16 v[36:39], v[148:151], v[196:199], v[36:39]
	v_mfma_f32_16x16x32_bf16 v[32:35], v[156:159], v[196:199], v[32:35]
	v_mfma_f32_16x16x32_bf16 v[20:23], v[148:151], v[222:225], v[20:23]
	v_mfma_f32_16x16x32_bf16 v[16:19], v[156:159], v[222:225], v[16:19]
	s_setprio 0
	s_setprio 1
	v_mfma_f32_16x16x32_bf16 v[44:47], v[160:163], v[176:179], 0
	v_mfma_f32_16x16x32_bf16 v[40:43], v[168:171], v[176:179], 0
	v_mfma_f32_16x16x32_bf16 v[28:31], v[160:163], v[184:187], 0
	v_mfma_f32_16x16x32_bf16 v[24:27], v[168:171], v[184:187], 0
	v_mfma_f32_16x16x32_bf16 v[12:15], v[160:163], v[192:195], 0
	v_mfma_f32_16x16x32_bf16 v[8:11], v[168:171], v[192:195], 0
	v_mfma_f32_16x16x32_bf16 v[4:7], v[160:163], v[200:203], 0
	v_mfma_f32_16x16x32_bf16 v[0:3], v[168:171], v[200:203], 0
	v_mfma_f32_16x16x32_bf16 v[44:47], v[164:167], v[180:183], v[44:47]
	v_mfma_f32_16x16x32_bf16 v[40:43], v[172:175], v[180:183], v[40:43]
	v_mfma_f32_16x16x32_bf16 v[28:31], v[164:167], v[188:191], v[28:31]
	v_mfma_f32_16x16x32_bf16 v[24:27], v[172:175], v[188:191], v[24:27]
	v_mfma_f32_16x16x32_bf16 v[12:15], v[164:167], v[196:199], v[12:15]
	v_mfma_f32_16x16x32_bf16 v[8:11], v[172:175], v[196:199], v[8:11]
	v_mfma_f32_16x16x32_bf16 v[4:7], v[164:167], v[222:225], v[4:7]
	v_mfma_f32_16x16x32_bf16 v[0:3], v[172:175], v[222:225], v[0:3]
	s_setprio 0
	s_barrier
	s_add_i32 s84, 0, 0x18000
	v_add_u32_e32 v96, s84, v141
	s_add_i32 s85, 0, 0x1c000
	ds_read_b128 v[144:147], v96
	ds_read_b128 v[148:151], v96 offset:1024
	ds_read_b128 v[152:155], v96 offset:2048
	ds_read_b128 v[156:159], v96 offset:3072
	v_add_u32_e32 v96, s85, v141
	ds_read_b128 v[160:163], v96
	ds_read_b128 v[164:167], v96 offset:1024
	ds_read_b128 v[168:171], v96 offset:2048
	ds_read_b128 v[172:175], v96 offset:3072
	s_add_u32 s82, s26, 0x80000
	v_mov_b32_e32 v96, v136
	s_mov_b32 m0, s38
	ds_read_b128 v[176:179], v142 offset:32768
	ds_read_b128 v[180:183], v142 offset:33792
	ds_read_b128 v[184:187], v142 offset:34816
	ds_read_b128 v[188:191], v142 offset:35840
	ds_read_b128 v[192:195], v142 offset:36864
	ds_read_b128 v[196:199], v142 offset:37888
	ds_read_b128 v[200:203], v142 offset:38912
	ds_read_b128 v[222:225], v142 offset:39936
	s_addc_u32 s83, s27, 0
	s_nop 0
	global_load_lds_dwordx4 v96, s[82:83]
	v_mov_b32_e32 v96, v138
	s_mov_b32 m0, s39
	s_nop 0
	global_load_lds_dwordx4 v96, s[82:83]
	s_waitcnt vmcnt(8)
	s_waitcnt lgkmcnt(0)
	s_barrier
	s_setprio 1
	s_waitcnt lgkmcnt(0)
	v_mfma_f32_16x16x32_bf16 v[126:129], v[144:147], v[176:179], v[126:129]
	v_mfma_f32_16x16x32_bf16 v[122:125], v[152:155], v[176:179], v[122:125]
	v_mfma_f32_16x16x32_bf16 v[118:121], v[144:147], v[184:187], v[118:121]
	v_mfma_f32_16x16x32_bf16 v[114:117], v[152:155], v[184:187], v[114:117]
	v_mfma_f32_16x16x32_bf16 v[102:105], v[144:147], v[192:195], v[102:105]
	v_mfma_f32_16x16x32_bf16 v[98:101], v[152:155], v[192:195], v[98:101]
	v_mfma_f32_16x16x32_bf16 v[84:87], v[144:147], v[200:203], v[84:87]
	v_mfma_f32_16x16x32_bf16 v[80:83], v[152:155], v[200:203], v[80:83]
	v_mfma_f32_16x16x32_bf16 v[126:129], v[148:151], v[180:183], v[126:129]
	v_mfma_f32_16x16x32_bf16 v[122:125], v[156:159], v[180:183], v[122:125]
	v_mfma_f32_16x16x32_bf16 v[118:121], v[148:151], v[188:191], v[118:121]
	v_mfma_f32_16x16x32_bf16 v[114:117], v[156:159], v[188:191], v[114:117]
	v_mfma_f32_16x16x32_bf16 v[102:105], v[148:151], v[196:199], v[102:105]
	v_mfma_f32_16x16x32_bf16 v[98:101], v[156:159], v[196:199], v[98:101]
	v_mfma_f32_16x16x32_bf16 v[84:87], v[148:151], v[222:225], v[84:87]
	v_mfma_f32_16x16x32_bf16 v[80:83], v[156:159], v[222:225], v[80:83]
	s_setprio 0
	s_setprio 1
	v_mfma_f32_16x16x32_bf16 v[110:113], v[160:163], v[176:179], v[110:113]
	v_mfma_f32_16x16x32_bf16 v[106:109], v[168:171], v[176:179], v[106:109]
	v_mfma_f32_16x16x32_bf16 v[92:95], v[160:163], v[184:187], v[92:95]
	v_mfma_f32_16x16x32_bf16 v[88:91], v[168:171], v[184:187], v[88:91]
	v_mfma_f32_16x16x32_bf16 v[76:79], v[160:163], v[192:195], v[76:79]
	v_mfma_f32_16x16x32_bf16 v[72:75], v[168:171], v[192:195], v[72:75]
	v_mfma_f32_16x16x32_bf16 v[68:71], v[160:163], v[200:203], v[68:71]
	v_mfma_f32_16x16x32_bf16 v[64:67], v[168:171], v[200:203], v[64:67]
	v_mfma_f32_16x16x32_bf16 v[110:113], v[164:167], v[180:183], v[110:113]
	v_mfma_f32_16x16x32_bf16 v[106:109], v[172:175], v[180:183], v[106:109]
	v_mfma_f32_16x16x32_bf16 v[92:95], v[164:167], v[188:191], v[92:95]
	v_mfma_f32_16x16x32_bf16 v[88:91], v[172:175], v[188:191], v[88:91]
	v_mfma_f32_16x16x32_bf16 v[76:79], v[164:167], v[196:199], v[76:79]
	v_mfma_f32_16x16x32_bf16 v[72:75], v[172:175], v[196:199], v[72:75]
	v_mfma_f32_16x16x32_bf16 v[68:71], v[164:167], v[222:225], v[68:71]
	v_mfma_f32_16x16x32_bf16 v[64:67], v[172:175], v[222:225], v[64:67]
	s_setprio 0
	s_barrier
	v_mov_b32_e32 v96, v137
	ds_read_b128 v[176:179], v142 offset:49152
	ds_read_b128 v[180:183], v142 offset:50176
	ds_read_b128 v[184:187], v142 offset:51200
	ds_read_b128 v[188:191], v142 offset:52224
	ds_read_b128 v[192:195], v142 offset:53248
	ds_read_b128 v[196:199], v142 offset:54272
	ds_read_b128 v[200:203], v142 offset:55296
	ds_read_b128 v[222:225], v142 offset:56320
	s_add_i32 s82, s84, s35
	v_lshl_add_u64 v[134:135], s[28:29], 0, v[96:97]
	v_lshl_add_u64 v[134:135], v[134:135], 0, s[0:1]
	s_mov_b32 m0, s82
	v_mov_b32_e32 v96, v139
	global_load_lds_dwordx4 v[134:135], off
	s_add_i32 m0, s82, 0x2000
	s_nop 0
	v_lshl_add_u64 v[134:135], s[28:29], 0, v[96:97]
	s_add_u32 s28, s28, 0x80080
	v_lshl_add_u64 v[134:135], v[134:135], 0, s[0:1]
	s_addc_u32 s29, s29, 0
	v_mov_b32_e32 v96, v137
	s_add_i32 s82, s85, s35
	global_load_lds_dwordx4 v[134:135], off
	s_mov_b32 m0, s82
	s_nop 0
	global_load_lds_dwordx4 v96, s[28:29]
	v_mov_b32_e32 v96, v139
	s_add_i32 m0, s82, 0x2000
	s_nop 0
	global_load_lds_dwordx4 v96, s[28:29]
	v_mov_b32_e32 v96, v136
	s_mov_b32 m0, s40
	v_lshl_add_u64 v[134:135], s[26:27], 0, v[96:97]
	v_lshl_add_u64 v[134:135], v[134:135], 0, s[0:1]
	v_mov_b32_e32 v96, v138
	global_load_lds_dwordx4 v[134:135], off
	s_mov_b32 m0, s41
	v_lshl_add_u64 v[134:135], s[26:27], 0, v[96:97]
	v_lshl_add_u64 v[134:135], v[134:135], 0, s[0:1]
	global_load_lds_dwordx4 v[134:135], off
	s_waitcnt vmcnt(8)
	s_waitcnt lgkmcnt(0)
	s_barrier
	s_setprio 1
	s_waitcnt lgkmcnt(0)
	v_mfma_f32_16x16x32_bf16 v[60:63], v[144:147], v[176:179], v[60:63]
	v_mfma_f32_16x16x32_bf16 v[56:59], v[152:155], v[176:179], v[56:59]
	v_mfma_f32_16x16x32_bf16 v[52:55], v[144:147], v[184:187], v[52:55]
	v_mfma_f32_16x16x32_bf16 v[48:51], v[152:155], v[184:187], v[48:51]
	v_mfma_f32_16x16x32_bf16 v[36:39], v[144:147], v[192:195], v[36:39]
	v_mfma_f32_16x16x32_bf16 v[32:35], v[152:155], v[192:195], v[32:35]
	v_mfma_f32_16x16x32_bf16 v[20:23], v[144:147], v[200:203], v[20:23]
	v_mfma_f32_16x16x32_bf16 v[16:19], v[152:155], v[200:203], v[16:19]
	v_mfma_f32_16x16x32_bf16 v[60:63], v[148:151], v[180:183], v[60:63]
	v_mfma_f32_16x16x32_bf16 v[56:59], v[156:159], v[180:183], v[56:59]
	v_mfma_f32_16x16x32_bf16 v[52:55], v[148:151], v[188:191], v[52:55]
	v_mfma_f32_16x16x32_bf16 v[48:51], v[156:159], v[188:191], v[48:51]
	v_mfma_f32_16x16x32_bf16 v[36:39], v[148:151], v[196:199], v[36:39]
	v_mfma_f32_16x16x32_bf16 v[32:35], v[156:159], v[196:199], v[32:35]
	v_mfma_f32_16x16x32_bf16 v[20:23], v[148:151], v[222:225], v[20:23]
	v_mfma_f32_16x16x32_bf16 v[16:19], v[156:159], v[222:225], v[16:19]
	s_setprio 0
	s_setprio 1
	v_mfma_f32_16x16x32_bf16 v[44:47], v[160:163], v[176:179], v[44:47]
	v_mfma_f32_16x16x32_bf16 v[40:43], v[168:171], v[176:179], v[40:43]
	v_mfma_f32_16x16x32_bf16 v[28:31], v[160:163], v[184:187], v[28:31]
	v_mfma_f32_16x16x32_bf16 v[24:27], v[168:171], v[184:187], v[24:27]
	v_mfma_f32_16x16x32_bf16 v[12:15], v[160:163], v[192:195], v[12:15]
	v_mfma_f32_16x16x32_bf16 v[8:11], v[168:171], v[192:195], v[8:11]
	v_mfma_f32_16x16x32_bf16 v[4:7], v[160:163], v[200:203], v[4:7]
	v_mfma_f32_16x16x32_bf16 v[0:3], v[168:171], v[200:203], v[0:3]
	v_mfma_f32_16x16x32_bf16 v[44:47], v[164:167], v[180:183], v[44:47]
	v_mfma_f32_16x16x32_bf16 v[40:43], v[172:175], v[180:183], v[40:43]
	v_mfma_f32_16x16x32_bf16 v[28:31], v[164:167], v[188:191], v[28:31]
	v_mfma_f32_16x16x32_bf16 v[24:27], v[172:175], v[188:191], v[24:27]
	v_mfma_f32_16x16x32_bf16 v[12:15], v[164:167], v[196:199], v[12:15]
	v_mfma_f32_16x16x32_bf16 v[8:11], v[172:175], v[196:199], v[8:11]
	v_mfma_f32_16x16x32_bf16 v[4:7], v[164:167], v[222:225], v[4:7]
	v_mfma_f32_16x16x32_bf16 v[0:3], v[172:175], v[222:225], v[0:3]
	s_setprio 0
	s_barrier
	s_add_i32 s81, s81, 2
	s_add_u32 s79, s79, 0x100
	s_addc_u32 s80, s80, 0
	s_add_u32 s24, s24, 0x100
	s_addc_u32 s25, s25, 0
	s_cmp_gt_u32 s81, 29
	s_cbranch_scc1 .Lmy_peel339_exit

.Lmy_peel339_exit:
	s_and_b64 vcc, exec, s[10:11]
	s_cbranch_vccz .LBB0_344
	s_barrier
	v_lshl_add_u32 v134, s78, 8, v140
	s_cmp_gt_i32 s47, 53
	s_mov_b64 s[20:21], -1
	s_cbranch_scc1 .LBB0_345

.LBB0_369:
	s_add_u32 s43, s22, 0x100
	s_addc_u32 s44, s23, 0
	s_add_u32 s20, s20, 0x80080
	s_addc_u32 s21, s21, 0
	s_mov_b32 s45, -2
	s_add_u32 s22, s20, 0xfff80080
	s_addc_u32 s23, s21, -1
	s_add_i32 s46, 0, 0x10000
	s_cmp_eq_u32 s45, 12
	s_cselect_b32 s23, s17, s23
	s_cselect_b32 s22, s16, s22
	v_add_u32_e32 v96, s46, v139
	s_cselect_b32 s25, s19, s44
	s_cselect_b32 s24, s18, s43
	s_add_i32 s78, 0, 0x14000
	ds_read_b128 v[142:145], v96
	ds_read_b128 v[146:149], v96 offset:1024
	ds_read_b128 v[150:153], v96 offset:2048
	ds_read_b128 v[154:157], v96 offset:3072
	v_add_u32_e32 v96, s78, v139
	ds_read_b128 v[158:161], v96
	ds_read_b128 v[162:165], v96 offset:1024
	ds_read_b128 v[166:169], v96 offset:2048
	ds_read_b128 v[170:173], v96 offset:3072
	v_mov_b32_e32 v96, v134
	ds_read_b128 v[174:177], v140
	ds_read_b128 v[178:181], v140 offset:1024
	ds_read_b128 v[182:185], v140 offset:2048
	ds_read_b128 v[186:189], v140 offset:3072
	ds_read_b128 v[190:193], v140 offset:4096
	ds_read_b128 v[194:197], v140 offset:5120
	ds_read_b128 v[222:225], v140 offset:6144
	ds_read_b128 v[226:229], v140 offset:7168
	s_add_i32 m0, s28, 0xc000
	s_nop 0
	global_load_lds_dwordx4 v96, s[20:21]
	v_mov_b32_e32 v96, v136
	s_add_i32 m0, s28, 0xe000
	s_nop 0
	global_load_lds_dwordx4 v96, s[20:21]
	s_waitcnt vmcnt(8)
	s_waitcnt lgkmcnt(0)
	s_barrier
	s_setprio 1
	s_waitcnt lgkmcnt(0)
	v_mfma_f32_16x16x128_f8f6f4 v[126:129], v[142:149], v[174:181], 0
	v_mfma_f32_16x16x128_f8f6f4 v[122:125], v[150:157], v[174:181], 0
	v_mfma_f32_16x16x128_f8f6f4 v[110:113], v[142:149], v[182:189], 0
	v_mfma_f32_16x16x128_f8f6f4 v[106:109], v[150:157], v[182:189], 0
	v_mfma_f32_16x16x128_f8f6f4 v[198:201], v[142:149], v[190:197], 0
	v_mfma_f32_16x16x128_f8f6f4 v[230:233], v[150:157], v[190:197], 0
	v_mfma_f32_16x16x128_f8f6f4 v[234:237], v[142:149], v[222:229], 0
	v_mfma_f32_16x16x128_f8f6f4 v[238:241], v[150:157], v[222:229], 0
	s_setprio 0
	s_setprio 1
	v_mfma_f32_16x16x128_f8f6f4 v[118:121], v[158:165], v[174:181], 0
	v_mfma_f32_16x16x128_f8f6f4 v[114:117], v[166:173], v[174:181], 0
	v_mfma_f32_16x16x128_f8f6f4 v[102:105], v[158:165], v[182:189], 0
	v_mfma_f32_16x16x128_f8f6f4 v[98:101], v[166:173], v[182:189], 0
	v_mfma_f32_16x16x128_f8f6f4 v[174:177], v[158:165], v[190:197], 0
	v_mfma_f32_16x16x128_f8f6f4 v[178:181], v[166:173], v[190:197], 0
	v_mfma_f32_16x16x128_f8f6f4 v[182:185], v[158:165], v[222:229], 0
	v_mfma_f32_16x16x128_f8f6f4 v[186:189], v[166:173], v[222:229], 0
	s_setprio 0
	s_barrier
	v_mov_b32_e32 v96, v135
	s_add_i32 s46, s46, s27
	s_nop 2
	ds_read_b128 v[64:67], v140 offset:16384
	ds_read_b128 v[68:71], v140 offset:17408
	ds_read_b128 v[72:75], v140 offset:18432
	ds_read_b128 v[76:79], v140 offset:19456
	ds_read_b128 v[80:83], v140 offset:20480
	ds_read_b128 v[84:87], v140 offset:21504
	ds_read_b128 v[88:91], v140 offset:22528
	ds_read_b128 v[92:95], v140 offset:23552
	s_mov_b32 m0, s46
	s_nop 0
	global_load_lds_dwordx4 v96, s[24:25]
	v_mov_b32_e32 v96, v137
	s_add_i32 m0, s46, 0x2000
	s_add_u32 s46, s24, 0x80000
	global_load_lds_dwordx4 v96, s[24:25]
	s_addc_u32 s47, s25, 0
	v_mov_b32_e32 v96, v135
	s_add_i32 s78, s78, s27
	s_mov_b32 m0, s78
	s_nop 0
	global_load_lds_dwordx4 v96, s[46:47]
	v_mov_b32_e32 v96, v137
	s_add_i32 m0, s78, 0x2000
	s_nop 0
	global_load_lds_dwordx4 v96, s[46:47]
	v_mov_b32_e32 v96, v134
	s_mov_b32 m0, s28
	s_nop 0
	global_load_lds_dwordx4 v96, s[22:23]
	v_mov_b32_e32 v96, v136
	s_mov_b32 m0, s29
	s_nop 0
	global_load_lds_dwordx4 v96, s[22:23]
	s_waitcnt vmcnt(8)
	s_waitcnt lgkmcnt(0)
	s_barrier
	s_setprio 1
	s_waitcnt lgkmcnt(0)
	v_mfma_f32_16x16x128_f8f6f4 v[60:63], v[142:149], v[64:71], 0
	v_mfma_f32_16x16x128_f8f6f4 v[56:59], v[150:157], v[64:71], 0
	v_mfma_f32_16x16x128_f8f6f4 v[190:193], v[142:149], v[72:79], 0
	v_mfma_f32_16x16x128_f8f6f4 v[194:197], v[150:157], v[72:79], 0
	v_mfma_f32_16x16x128_f8f6f4 v[222:225], v[142:149], v[80:87], 0
	v_mfma_f32_16x16x128_f8f6f4 v[226:229], v[150:157], v[80:87], 0
	v_mfma_f32_16x16x128_f8f6f4 v[242:245], v[142:149], v[88:95], 0
	v_mfma_f32_16x16x128_f8f6f4 v[246:249], v[150:157], v[88:95], 0
	s_setprio 0
	s_setprio 1
	v_mfma_f32_16x16x128_f8f6f4 v[52:55], v[158:165], v[64:71], 0
	v_mfma_f32_16x16x128_f8f6f4 v[48:51], v[166:173], v[64:71], 0
	v_mfma_f32_16x16x128_f8f6f4 v[250:253], v[158:165], v[72:79], 0
	v_mfma_f32_16x16x128_f8f6f4 v[208:211], v[166:173], v[72:79], 0
	v_mfma_f32_16x16x128_f8f6f4 v[218:221], v[158:165], v[80:87], 0
	v_mfma_f32_16x16x128_f8f6f4 v[202:205], v[166:173], v[80:87], 0
	v_mfma_f32_16x16x128_f8f6f4 v[212:215], v[158:165], v[88:95], 0
	v_mfma_f32_16x16x128_f8f6f4 v[130:133], v[166:173], v[88:95], 0
	s_setprio 0
	s_barrier
	s_add_i32 s78, 0, 0x18000
	v_add_u32_e32 v8, s78, v139
	s_add_i32 s79, 0, 0x1c000
	s_nop 1
	ds_read_b128 v[0:3], v8
	ds_read_b128 v[4:7], v8 offset:1024
	ds_read_b128 v[16:19], v8 offset:2048
	ds_read_b128 v[20:23], v8 offset:3072
	v_add_u32_e32 v8, s79, v139
	ds_read_b128 v[142:145], v8
	ds_read_b128 v[146:149], v8 offset:1024
	ds_read_b128 v[150:153], v8 offset:2048
	ds_read_b128 v[154:157], v8 offset:3072
	s_add_u32 s46, s22, 0x80000
	v_mov_b32_e32 v64, v134
	s_mov_b32 m0, s30
	ds_read_b128 v[8:11], v140 offset:32768
	ds_read_b128 v[12:15], v140 offset:33792
	ds_read_b128 v[24:27], v140 offset:34816
	ds_read_b128 v[28:31], v140 offset:35840
	ds_read_b128 v[32:35], v140 offset:36864
	ds_read_b128 v[36:39], v140 offset:37888
	ds_read_b128 v[40:43], v140 offset:38912
	ds_read_b128 v[44:47], v140 offset:39936
	s_addc_u32 s47, s23, 0
	s_nop 0
	global_load_lds_dwordx4 v64, s[46:47]
	v_mov_b32_e32 v64, v136
	s_mov_b32 m0, s31
	s_nop 0
	global_load_lds_dwordx4 v64, s[46:47]
	s_waitcnt vmcnt(8)
	s_waitcnt lgkmcnt(0)
	s_barrier
	s_setprio 1
	s_waitcnt lgkmcnt(0)
	v_mfma_f32_16x16x128_f8f6f4 v[126:129], v[0:7], v[8:15], v[126:129]
	v_mfma_f32_16x16x128_f8f6f4 v[122:125], v[16:23], v[8:15], v[122:125]
	v_mfma_f32_16x16x128_f8f6f4 v[110:113], v[0:7], v[24:31], v[110:113]
	v_mfma_f32_16x16x128_f8f6f4 v[106:109], v[16:23], v[24:31], v[106:109]
	v_mfma_f32_16x16x128_f8f6f4 v[92:95], v[0:7], v[32:39], v[198:201]
	v_mfma_f32_16x16x128_f8f6f4 v[88:91], v[16:23], v[32:39], v[230:233]
	v_mfma_f32_16x16x128_f8f6f4 v[76:79], v[0:7], v[40:47], v[234:237]
	v_mfma_f32_16x16x128_f8f6f4 v[72:75], v[16:23], v[40:47], v[238:241]
	s_setprio 0
	s_setprio 1
	v_mfma_f32_16x16x128_f8f6f4 v[118:121], v[142:149], v[8:15], v[118:121]
	v_mfma_f32_16x16x128_f8f6f4 v[114:117], v[150:157], v[8:15], v[114:117]
	v_mfma_f32_16x16x128_f8f6f4 v[102:105], v[142:149], v[24:31], v[102:105]
	v_mfma_f32_16x16x128_f8f6f4 v[98:101], v[150:157], v[24:31], v[98:101]
	v_mfma_f32_16x16x128_f8f6f4 v[84:87], v[142:149], v[32:39], v[174:177]
	v_mfma_f32_16x16x128_f8f6f4 v[80:83], v[150:157], v[32:39], v[178:181]
	v_mfma_f32_16x16x128_f8f6f4 v[68:71], v[142:149], v[40:47], v[182:185]
	v_mfma_f32_16x16x128_f8f6f4 v[64:67], v[150:157], v[40:47], v[186:189]
	s_setprio 0
	s_barrier
	v_mov_b32_e32 v96, v135
	ds_read_b128 v[32:35], v140 offset:49152
	ds_read_b128 v[36:39], v140 offset:50176
	ds_read_b128 v[158:161], v140 offset:51200
	ds_read_b128 v[162:165], v140 offset:52224
	ds_read_b128 v[166:169], v140 offset:53248
	ds_read_b128 v[170:173], v140 offset:54272
	ds_read_b128 v[174:177], v140 offset:55296
	ds_read_b128 v[178:181], v140 offset:56320
	s_add_i32 s46, s78, s27
	v_lshl_add_u64 v[8:9], s[24:25], 0, v[96:97]
	v_lshl_add_u64 v[8:9], v[8:9], 0, s[0:1]
	s_mov_b32 m0, s46
	v_mov_b32_e32 v96, v137
	global_load_lds_dwordx4 v[8:9], off
	s_add_i32 m0, s46, 0x2000
	v_lshl_add_u64 v[8:9], s[24:25], 0, v[96:97]
	v_lshl_add_u64 v[8:9], v[8:9], 0, s[0:1]
	s_add_u32 s24, s24, 0x80080
	global_load_lds_dwordx4 v[8:9], off
	s_addc_u32 s25, s25, 0
	v_mov_b32_e32 v8, v135
	s_add_i32 s46, s79, s27
	s_mov_b32 m0, s46
	v_mov_b32_e32 v96, v134
	global_load_lds_dwordx4 v8, s[24:25]
	v_mov_b32_e32 v8, v137
	s_add_i32 m0, s46, 0x2000
	s_nop 0
	global_load_lds_dwordx4 v8, s[24:25]
	s_mov_b32 m0, s34
	v_lshl_add_u64 v[8:9], s[22:23], 0, v[96:97]
	v_lshl_add_u64 v[8:9], v[8:9], 0, s[0:1]
	v_mov_b32_e32 v96, v136
	global_load_lds_dwordx4 v[8:9], off
	s_mov_b32 m0, s35
	v_lshl_add_u64 v[8:9], s[22:23], 0, v[96:97]
	v_lshl_add_u64 v[8:9], v[8:9], 0, s[0:1]
	global_load_lds_dwordx4 v[8:9], off
	s_waitcnt vmcnt(8)
	s_waitcnt lgkmcnt(0)
	s_barrier
	s_setprio 1
	s_waitcnt lgkmcnt(0)
	v_mfma_f32_16x16x128_f8f6f4 v[60:63], v[0:7], v[32:39], v[60:63]
	v_mfma_f32_16x16x128_f8f6f4 v[56:59], v[16:23], v[32:39], v[56:59]
	v_mfma_f32_16x16x128_f8f6f4 v[44:47], v[0:7], v[158:165], v[190:193]
	v_mfma_f32_16x16x128_f8f6f4 v[40:43], v[16:23], v[158:165], v[194:197]
	v_mfma_f32_16x16x128_f8f6f4 v[28:31], v[0:7], v[166:173], v[222:225]
	v_mfma_f32_16x16x128_f8f6f4 v[24:27], v[16:23], v[166:173], v[226:229]
	v_mfma_f32_16x16x128_f8f6f4 v[12:15], v[0:7], v[174:181], v[242:245]
	v_mfma_f32_16x16x128_f8f6f4 v[8:11], v[16:23], v[174:181], v[246:249]
	s_setprio 0
	s_setprio 1
	v_mfma_f32_16x16x128_f8f6f4 v[52:55], v[142:149], v[32:39], v[52:55]
	v_mfma_f32_16x16x128_f8f6f4 v[48:51], v[150:157], v[32:39], v[48:51]
	v_mfma_f32_16x16x128_f8f6f4 v[36:39], v[142:149], v[158:165], v[250:253]
	v_mfma_f32_16x16x128_f8f6f4 v[32:35], v[150:157], v[158:165], v[208:211]
	v_mfma_f32_16x16x128_f8f6f4 v[20:23], v[142:149], v[166:173], v[218:221]
	v_mfma_f32_16x16x128_f8f6f4 v[16:19], v[150:157], v[166:173], v[202:205]
	v_mfma_f32_16x16x128_f8f6f4 v[4:7], v[142:149], v[174:181], v[212:215]
	v_mfma_f32_16x16x128_f8f6f4 v[0:3], v[150:157], v[174:181], v[130:133]
	s_setprio 0
	s_barrier
	s_add_i32 s45, s45, 2
	s_add_u32 s43, s43, 0x100
	s_addc_u32 s44, s44, 0
	s_add_u32 s20, s20, 0x100
	s_addc_u32 s21, s21, 0
	s_cmp_gt_u32 s45, 13
	s_cbranch_scc1 .Lmy_peel370_exit

.Lmy_peel370_exit:
	s_and_b64 vcc, exec, s[8:9]
	s_cbranch_vccz .LBB0_373
	s_barrier

.LBB0_1369:
	s_add_u32 s79, s26, 0x100
	s_addc_u32 s80, s27, 0
	s_add_u32 s24, s24, 0x80080
	s_addc_u32 s25, s25, 0
	s_mov_b32 s81, -2
	s_waitcnt vmcnt(0)
	s_add_u32 s26, s24, 0xfff80080
	s_addc_u32 s27, s25, -1
	s_add_i32 s82, 0, 0x10000
	s_cmp_eq_u32 s81, 28
	s_cselect_b32 s27, s21, s27
	s_cselect_b32 s26, s20, s26
	v_add_u32_e32 v96, s82, v155
	s_cselect_b32 s29, s23, s80
	s_cselect_b32 s28, s22, s79
	s_add_i32 s84, 0, 0x14000
	ds_read_b128 v[130:133], v96
	ds_read_b128 v[134:137], v96 offset:1024
	ds_read_b128 v[138:141], v96 offset:2048
	ds_read_b128 v[142:145], v96 offset:3072
	v_add_u32_e32 v96, s84, v155
	ds_read_b128 v[146:149], v96
	ds_read_b128 v[158:161], v96 offset:1024
	ds_read_b128 v[162:165], v96 offset:2048
	ds_read_b128 v[166:169], v96 offset:3072
	v_mov_b32_e32 v96, v152
	ds_read_b128 v[170:173], v157
	ds_read_b128 v[174:177], v157 offset:1024
	ds_read_b128 v[178:181], v157 offset:2048
	ds_read_b128 v[182:185], v157 offset:3072
	ds_read_b128 v[186:189], v157 offset:4096
	ds_read_b128 v[190:193], v157 offset:5120
	ds_read_b128 v[194:197], v157 offset:6144
	ds_read_b128 v[198:201], v157 offset:7168
	s_add_i32 m0, s35, 0xc000
	s_nop 0
	global_load_lds_dwordx4 v96, s[24:25]
	v_mov_b32_e32 v96, v153
	s_add_i32 m0, s35, 0xe000
	s_nop 0
	global_load_lds_dwordx4 v96, s[24:25]
	s_waitcnt vmcnt(8)
	s_waitcnt lgkmcnt(0)
	s_barrier
	s_setprio 1
	s_waitcnt lgkmcnt(0)
	v_mfma_f32_16x16x32_bf16 v[126:129], v[130:133], v[170:173], 0
	v_mfma_f32_16x16x32_bf16 v[122:125], v[138:141], v[170:173], 0
	v_mfma_f32_16x16x32_bf16 v[114:117], v[130:133], v[178:181], 0
	v_mfma_f32_16x16x32_bf16 v[110:113], v[138:141], v[178:181], 0
	v_mfma_f32_16x16x32_bf16 v[98:101], v[130:133], v[186:189], 0
	v_mfma_f32_16x16x32_bf16 v[92:95], v[138:141], v[186:189], 0
	v_mfma_f32_16x16x32_bf16 v[80:83], v[130:133], v[194:197], 0
	v_mfma_f32_16x16x32_bf16 v[76:79], v[138:141], v[194:197], 0
	v_mfma_f32_16x16x32_bf16 v[126:129], v[134:137], v[174:177], v[126:129]
	v_mfma_f32_16x16x32_bf16 v[122:125], v[142:145], v[174:177], v[122:125]
	v_mfma_f32_16x16x32_bf16 v[114:117], v[134:137], v[182:185], v[114:117]
	v_mfma_f32_16x16x32_bf16 v[110:113], v[142:145], v[182:185], v[110:113]
	v_mfma_f32_16x16x32_bf16 v[98:101], v[134:137], v[190:193], v[98:101]
	v_mfma_f32_16x16x32_bf16 v[92:95], v[142:145], v[190:193], v[92:95]
	v_mfma_f32_16x16x32_bf16 v[80:83], v[134:137], v[198:201], v[80:83]
	v_mfma_f32_16x16x32_bf16 v[76:79], v[142:145], v[198:201], v[76:79]
	s_setprio 0
	s_setprio 1
	v_mfma_f32_16x16x32_bf16 v[118:121], v[146:149], v[170:173], 0
	v_mfma_f32_16x16x32_bf16 v[106:109], v[162:165], v[170:173], 0
	v_mfma_f32_16x16x32_bf16 v[102:105], v[146:149], v[178:181], 0
	v_mfma_f32_16x16x32_bf16 v[88:91], v[162:165], v[178:181], 0
	v_mfma_f32_16x16x32_bf16 v[84:87], v[146:149], v[186:189], 0
	v_mfma_f32_16x16x32_bf16 v[72:75], v[162:165], v[186:189], 0
	v_mfma_f32_16x16x32_bf16 v[68:71], v[146:149], v[194:197], 0
	v_mfma_f32_16x16x32_bf16 v[60:63], v[162:165], v[194:197], 0
	v_mfma_f32_16x16x32_bf16 v[118:121], v[158:161], v[174:177], v[118:121]
	v_mfma_f32_16x16x32_bf16 v[106:109], v[166:169], v[174:177], v[106:109]
	v_mfma_f32_16x16x32_bf16 v[102:105], v[158:161], v[182:185], v[102:105]
	v_mfma_f32_16x16x32_bf16 v[88:91], v[166:169], v[182:185], v[88:91]
	v_mfma_f32_16x16x32_bf16 v[84:87], v[158:161], v[190:193], v[84:87]
	v_mfma_f32_16x16x32_bf16 v[72:75], v[166:169], v[190:193], v[72:75]
	v_mfma_f32_16x16x32_bf16 v[68:71], v[158:161], v[198:201], v[68:71]
	v_mfma_f32_16x16x32_bf16 v[60:63], v[166:169], v[198:201], v[60:63]
	s_setprio 0
	s_barrier
	v_mov_b32_e32 v96, v152
	s_add_i32 s82, s82, s34
	ds_read_b128 v[170:173], v157 offset:16384
	ds_read_b128 v[174:177], v157 offset:17408
	ds_read_b128 v[178:181], v157 offset:18432
	ds_read_b128 v[182:185], v157 offset:19456
	ds_read_b128 v[186:189], v157 offset:20480
	ds_read_b128 v[190:193], v157 offset:21504
	ds_read_b128 v[194:197], v157 offset:22528
	ds_read_b128 v[198:201], v157 offset:23552
	s_mov_b32 m0, s82
	s_nop 0
	global_load_lds_dwordx4 v96, s[28:29]
	v_mov_b32_e32 v96, v153
	s_add_i32 m0, s82, 0x2000
	s_add_u32 s82, s28, 0x80000
	global_load_lds_dwordx4 v96, s[28:29]
	s_addc_u32 s83, s29, 0
	v_mov_b32_e32 v96, v152
	s_add_i32 s84, s84, s34
	s_mov_b32 m0, s84
	s_nop 0
	global_load_lds_dwordx4 v96, s[82:83]
	v_mov_b32_e32 v96, v153
	s_add_i32 m0, s84, 0x2000
	s_nop 0
	global_load_lds_dwordx4 v96, s[82:83]
	v_mov_b32_e32 v96, v152
	s_mov_b32 m0, s35
	s_nop 0
	global_load_lds_dwordx4 v96, s[26:27]
	v_mov_b32_e32 v96, v153
	s_mov_b32 m0, s36
	s_nop 0
	global_load_lds_dwordx4 v96, s[26:27]
	s_waitcnt vmcnt(8)
	s_waitcnt lgkmcnt(0)
	s_barrier
	s_setprio 1
	s_waitcnt lgkmcnt(0)
	v_mfma_f32_16x16x32_bf16 v[64:67], v[130:133], v[170:173], 0
	v_mfma_f32_16x16x32_bf16 v[56:59], v[138:141], v[170:173], 0
	v_mfma_f32_16x16x32_bf16 v[48:51], v[130:133], v[178:181], 0
	v_mfma_f32_16x16x32_bf16 v[44:47], v[138:141], v[178:181], 0
	v_mfma_f32_16x16x32_bf16 v[32:35], v[130:133], v[186:189], 0
	v_mfma_f32_16x16x32_bf16 v[28:31], v[138:141], v[186:189], 0
	v_mfma_f32_16x16x32_bf16 v[16:19], v[130:133], v[194:197], 0
	v_mfma_f32_16x16x32_bf16 v[12:15], v[138:141], v[194:197], 0
	v_mfma_f32_16x16x32_bf16 v[64:67], v[134:137], v[174:177], v[64:67]
	v_mfma_f32_16x16x32_bf16 v[56:59], v[142:145], v[174:177], v[56:59]
	v_mfma_f32_16x16x32_bf16 v[48:51], v[134:137], v[182:185], v[48:51]
	v_mfma_f32_16x16x32_bf16 v[44:47], v[142:145], v[182:185], v[44:47]
	v_mfma_f32_16x16x32_bf16 v[32:35], v[134:137], v[190:193], v[32:35]
	v_mfma_f32_16x16x32_bf16 v[28:31], v[142:145], v[190:193], v[28:31]
	v_mfma_f32_16x16x32_bf16 v[16:19], v[134:137], v[198:201], v[16:19]
	v_mfma_f32_16x16x32_bf16 v[12:15], v[142:145], v[198:201], v[12:15]
	s_setprio 0
	s_setprio 1
	v_mfma_f32_16x16x32_bf16 v[52:55], v[146:149], v[170:173], 0
	v_mfma_f32_16x16x32_bf16 v[40:43], v[162:165], v[170:173], 0
	v_mfma_f32_16x16x32_bf16 v[36:39], v[146:149], v[178:181], 0
	v_mfma_f32_16x16x32_bf16 v[24:27], v[162:165], v[178:181], 0
	v_mfma_f32_16x16x32_bf16 v[20:23], v[146:149], v[186:189], 0
	v_mfma_f32_16x16x32_bf16 v[8:11], v[162:165], v[186:189], 0
	v_mfma_f32_16x16x32_bf16 v[4:7], v[146:149], v[194:197], 0
	v_mfma_f32_16x16x32_bf16 v[0:3], v[162:165], v[194:197], 0
	v_mfma_f32_16x16x32_bf16 v[52:55], v[158:161], v[174:177], v[52:55]
	v_mfma_f32_16x16x32_bf16 v[40:43], v[166:169], v[174:177], v[40:43]
	v_mfma_f32_16x16x32_bf16 v[36:39], v[158:161], v[182:185], v[36:39]
	v_mfma_f32_16x16x32_bf16 v[24:27], v[166:169], v[182:185], v[24:27]
	v_mfma_f32_16x16x32_bf16 v[20:23], v[158:161], v[190:193], v[20:23]
	v_mfma_f32_16x16x32_bf16 v[8:11], v[166:169], v[190:193], v[8:11]
	v_mfma_f32_16x16x32_bf16 v[4:7], v[158:161], v[198:201], v[4:7]
	v_mfma_f32_16x16x32_bf16 v[0:3], v[166:169], v[198:201], v[0:3]
	s_setprio 0
	s_barrier
	s_add_i32 s84, 0, 0x18000
	v_add_u32_e32 v96, s84, v155
	s_add_i32 s85, 0, 0x1c000
	ds_read_b128 v[130:133], v96
	ds_read_b128 v[134:137], v96 offset:1024
	ds_read_b128 v[138:141], v96 offset:2048
	ds_read_b128 v[142:145], v96 offset:3072
	v_add_u32_e32 v96, s85, v155
	ds_read_b128 v[146:149], v96
	ds_read_b128 v[158:161], v96 offset:1024
	ds_read_b128 v[162:165], v96 offset:2048
	ds_read_b128 v[166:169], v96 offset:3072
	s_add_u32 s82, s26, 0x80000
	v_mov_b32_e32 v96, v152
	s_mov_b32 m0, s37
	ds_read_b128 v[170:173], v157 offset:32768
	ds_read_b128 v[174:177], v157 offset:33792
	ds_read_b128 v[178:181], v157 offset:34816
	ds_read_b128 v[182:185], v157 offset:35840
	ds_read_b128 v[186:189], v157 offset:36864
	ds_read_b128 v[190:193], v157 offset:37888
	ds_read_b128 v[194:197], v157 offset:38912
	ds_read_b128 v[198:201], v157 offset:39936
	s_addc_u32 s83, s27, 0
	s_nop 0
	global_load_lds_dwordx4 v96, s[82:83]
	v_mov_b32_e32 v96, v153
	s_mov_b32 m0, s38
	s_nop 0
	global_load_lds_dwordx4 v96, s[82:83]
	s_waitcnt vmcnt(8)
	s_waitcnt lgkmcnt(0)
	s_barrier
	s_setprio 1
	s_waitcnt lgkmcnt(0)
	v_mfma_f32_16x16x32_bf16 v[126:129], v[130:133], v[170:173], v[126:129]
	v_mfma_f32_16x16x32_bf16 v[122:125], v[138:141], v[170:173], v[122:125]
	v_mfma_f32_16x16x32_bf16 v[114:117], v[130:133], v[178:181], v[114:117]
	v_mfma_f32_16x16x32_bf16 v[110:113], v[138:141], v[178:181], v[110:113]
	v_mfma_f32_16x16x32_bf16 v[98:101], v[130:133], v[186:189], v[98:101]
	v_mfma_f32_16x16x32_bf16 v[92:95], v[138:141], v[186:189], v[92:95]
	v_mfma_f32_16x16x32_bf16 v[80:83], v[130:133], v[194:197], v[80:83]
	v_mfma_f32_16x16x32_bf16 v[76:79], v[138:141], v[194:197], v[76:79]
	v_mfma_f32_16x16x32_bf16 v[126:129], v[134:137], v[174:177], v[126:129]
	v_mfma_f32_16x16x32_bf16 v[122:125], v[142:145], v[174:177], v[122:125]
	v_mfma_f32_16x16x32_bf16 v[114:117], v[134:137], v[182:185], v[114:117]
	v_mfma_f32_16x16x32_bf16 v[110:113], v[142:145], v[182:185], v[110:113]
	v_mfma_f32_16x16x32_bf16 v[98:101], v[134:137], v[190:193], v[98:101]
	v_mfma_f32_16x16x32_bf16 v[92:95], v[142:145], v[190:193], v[92:95]
	v_mfma_f32_16x16x32_bf16 v[80:83], v[134:137], v[198:201], v[80:83]
	v_mfma_f32_16x16x32_bf16 v[76:79], v[142:145], v[198:201], v[76:79]
	s_setprio 0
	s_setprio 1
	v_mfma_f32_16x16x32_bf16 v[118:121], v[146:149], v[170:173], v[118:121]
	v_mfma_f32_16x16x32_bf16 v[106:109], v[162:165], v[170:173], v[106:109]
	v_mfma_f32_16x16x32_bf16 v[102:105], v[146:149], v[178:181], v[102:105]
	v_mfma_f32_16x16x32_bf16 v[88:91], v[162:165], v[178:181], v[88:91]
	v_mfma_f32_16x16x32_bf16 v[84:87], v[146:149], v[186:189], v[84:87]
	v_mfma_f32_16x16x32_bf16 v[72:75], v[162:165], v[186:189], v[72:75]
	v_mfma_f32_16x16x32_bf16 v[68:71], v[146:149], v[194:197], v[68:71]
	v_mfma_f32_16x16x32_bf16 v[60:63], v[162:165], v[194:197], v[60:63]
	v_mfma_f32_16x16x32_bf16 v[118:121], v[158:161], v[174:177], v[118:121]
	v_mfma_f32_16x16x32_bf16 v[106:109], v[166:169], v[174:177], v[106:109]
	v_mfma_f32_16x16x32_bf16 v[102:105], v[158:161], v[182:185], v[102:105]
	v_mfma_f32_16x16x32_bf16 v[88:91], v[166:169], v[182:185], v[88:91]
	v_mfma_f32_16x16x32_bf16 v[84:87], v[158:161], v[190:193], v[84:87]
	v_mfma_f32_16x16x32_bf16 v[72:75], v[166:169], v[190:193], v[72:75]
	v_mfma_f32_16x16x32_bf16 v[68:71], v[158:161], v[198:201], v[68:71]
	v_mfma_f32_16x16x32_bf16 v[60:63], v[166:169], v[198:201], v[60:63]
	s_setprio 0
	s_barrier
	v_mov_b32_e32 v96, v152
	ds_read_b128 v[170:173], v157 offset:49152
	ds_read_b128 v[174:177], v157 offset:50176
	ds_read_b128 v[178:181], v157 offset:51200
	ds_read_b128 v[182:185], v157 offset:52224
	ds_read_b128 v[186:189], v157 offset:53248
	ds_read_b128 v[190:193], v157 offset:54272
	ds_read_b128 v[194:197], v157 offset:55296
	ds_read_b128 v[198:201], v157 offset:56320
	s_add_i32 s82, s84, s34
	v_lshl_add_u64 v[150:151], s[28:29], 0, v[96:97]
	v_lshl_add_u64 v[150:151], v[150:151], 0, s[0:1]
	s_mov_b32 m0, s82
	v_mov_b32_e32 v96, v153
	global_load_lds_dwordx4 v[150:151], off
	s_add_i32 m0, s82, 0x2000
	s_nop 0
	v_lshl_add_u64 v[150:151], s[28:29], 0, v[96:97]
	s_add_u32 s28, s28, 0x80080
	v_lshl_add_u64 v[150:151], v[150:151], 0, s[0:1]
	s_addc_u32 s29, s29, 0
	v_mov_b32_e32 v96, v152
	s_add_i32 s82, s85, s34
	global_load_lds_dwordx4 v[150:151], off
	s_mov_b32 m0, s82
	s_nop 0
	global_load_lds_dwordx4 v96, s[28:29]
	v_mov_b32_e32 v96, v153
	s_add_i32 m0, s82, 0x2000
	s_nop 0
	global_load_lds_dwordx4 v96, s[28:29]
	v_mov_b32_e32 v96, v152
	s_mov_b32 m0, s40
	v_lshl_add_u64 v[150:151], s[26:27], 0, v[96:97]
	v_lshl_add_u64 v[150:151], v[150:151], 0, s[0:1]
	v_mov_b32_e32 v96, v153
	global_load_lds_dwordx4 v[150:151], off
	s_mov_b32 m0, s41
	v_lshl_add_u64 v[150:151], s[26:27], 0, v[96:97]
	v_lshl_add_u64 v[150:151], v[150:151], 0, s[0:1]
	global_load_lds_dwordx4 v[150:151], off
	s_waitcnt vmcnt(8)
	s_waitcnt lgkmcnt(0)
	s_barrier
	s_setprio 1
	s_waitcnt lgkmcnt(0)
	v_mfma_f32_16x16x32_bf16 v[64:67], v[130:133], v[170:173], v[64:67]
	v_mfma_f32_16x16x32_bf16 v[56:59], v[138:141], v[170:173], v[56:59]
	v_mfma_f32_16x16x32_bf16 v[48:51], v[130:133], v[178:181], v[48:51]
	v_mfma_f32_16x16x32_bf16 v[44:47], v[138:141], v[178:181], v[44:47]
	v_mfma_f32_16x16x32_bf16 v[32:35], v[130:133], v[186:189], v[32:35]
	v_mfma_f32_16x16x32_bf16 v[28:31], v[138:141], v[186:189], v[28:31]
	v_mfma_f32_16x16x32_bf16 v[16:19], v[130:133], v[194:197], v[16:19]
	v_mfma_f32_16x16x32_bf16 v[12:15], v[138:141], v[194:197], v[12:15]
	v_mfma_f32_16x16x32_bf16 v[64:67], v[134:137], v[174:177], v[64:67]
	v_mfma_f32_16x16x32_bf16 v[56:59], v[142:145], v[174:177], v[56:59]
	v_mfma_f32_16x16x32_bf16 v[48:51], v[134:137], v[182:185], v[48:51]
	v_mfma_f32_16x16x32_bf16 v[44:47], v[142:145], v[182:185], v[44:47]
	v_mfma_f32_16x16x32_bf16 v[32:35], v[134:137], v[190:193], v[32:35]
	v_mfma_f32_16x16x32_bf16 v[28:31], v[142:145], v[190:193], v[28:31]
	v_mfma_f32_16x16x32_bf16 v[16:19], v[134:137], v[198:201], v[16:19]
	v_mfma_f32_16x16x32_bf16 v[12:15], v[142:145], v[198:201], v[12:15]
	s_setprio 0
	s_setprio 1
	v_mfma_f32_16x16x32_bf16 v[52:55], v[146:149], v[170:173], v[52:55]
	v_mfma_f32_16x16x32_bf16 v[40:43], v[162:165], v[170:173], v[40:43]
	v_mfma_f32_16x16x32_bf16 v[36:39], v[146:149], v[178:181], v[36:39]
	v_mfma_f32_16x16x32_bf16 v[24:27], v[162:165], v[178:181], v[24:27]
	v_mfma_f32_16x16x32_bf16 v[20:23], v[146:149], v[186:189], v[20:23]
	v_mfma_f32_16x16x32_bf16 v[8:11], v[162:165], v[186:189], v[8:11]
	v_mfma_f32_16x16x32_bf16 v[4:7], v[146:149], v[194:197], v[4:7]
	v_mfma_f32_16x16x32_bf16 v[0:3], v[162:165], v[194:197], v[0:3]
	v_mfma_f32_16x16x32_bf16 v[52:55], v[158:161], v[174:177], v[52:55]
	v_mfma_f32_16x16x32_bf16 v[40:43], v[166:169], v[174:177], v[40:43]
	v_mfma_f32_16x16x32_bf16 v[36:39], v[158:161], v[182:185], v[36:39]
	v_mfma_f32_16x16x32_bf16 v[24:27], v[166:169], v[182:185], v[24:27]
	v_mfma_f32_16x16x32_bf16 v[20:23], v[158:161], v[190:193], v[20:23]
	v_mfma_f32_16x16x32_bf16 v[8:11], v[166:169], v[190:193], v[8:11]
	v_mfma_f32_16x16x32_bf16 v[4:7], v[158:161], v[198:201], v[4:7]
	v_mfma_f32_16x16x32_bf16 v[0:3], v[166:169], v[198:201], v[0:3]
	s_setprio 0
	s_barrier
	s_add_i32 s81, s81, 2
	s_add_u32 s79, s79, 0x100
	s_addc_u32 s80, s80, 0
	s_add_u32 s24, s24, 0x100
	s_addc_u32 s25, s25, 0
	s_cmp_gt_u32 s81, 29
	s_cbranch_scc1 .Lmy_peel1370_exit

.Lmy_peel1370_exit:
	s_and_b64 vcc, exec, s[14:15]
	s_cbranch_vccz .LBB0_1373
	s_barrier

.LBB0_1782:
	s_add_u32 s43, s20, 0x100
	s_addc_u32 s46, s21, 0
	s_add_u32 s18, s18, 0x80080
	s_addc_u32 s19, s19, 0
	s_mov_b32 s47, -2
	s_add_u32 s20, s18, 0xfff80080
	s_addc_u32 s21, s19, -1
	s_add_i32 s76, 0, 0x10000
	s_cmp_eq_u32 s47, 28
	s_cselect_b32 s21, s15, s21
	s_cselect_b32 s20, s14, s20
	v_add_u32_e32 v96, s76, v138
	s_cselect_b32 s23, s17, s46
	s_cselect_b32 s22, s16, s43
	s_add_i32 s80, 0, 0x14000
	ds_read_b128 v[142:145], v96
	ds_read_b128 v[146:149], v96 offset:1024
	ds_read_b128 v[150:153], v96 offset:2048
	ds_read_b128 v[154:157], v96 offset:3072
	v_add_u32_e32 v96, s80, v138
	ds_read_b128 v[158:161], v96
	ds_read_b128 v[162:165], v96 offset:1024
	ds_read_b128 v[166:169], v96 offset:2048
	ds_read_b128 v[170:173], v96 offset:3072
	v_mov_b32_e32 v96, v131
	ds_read_b128 v[174:177], v140
	ds_read_b128 v[178:181], v140 offset:1024
	ds_read_b128 v[182:185], v140 offset:2048
	ds_read_b128 v[186:189], v140 offset:3072
	ds_read_b128 v[190:193], v140 offset:4096
	ds_read_b128 v[194:197], v140 offset:5120
	ds_read_b128 v[198:201], v140 offset:6144
	ds_read_b128 v[202:205], v140 offset:7168
	s_add_i32 m0, s26, 0xc000
	s_nop 0
	global_load_lds_dwordx4 v96, s[18:19]
	v_mov_b32_e32 v96, v135
	s_add_i32 m0, s26, 0xe000
	s_nop 0
	global_load_lds_dwordx4 v96, s[18:19]
	s_waitcnt vmcnt(8)
	s_waitcnt lgkmcnt(0)
	s_barrier
	s_setprio 1
	s_waitcnt lgkmcnt(0)
	v_mfma_f32_16x16x32_bf16 v[126:129], v[142:145], v[174:177], 0
	v_mfma_f32_16x16x32_bf16 v[118:121], v[150:153], v[174:177], 0
	v_mfma_f32_16x16x32_bf16 v[110:113], v[142:145], v[182:185], 0
	v_mfma_f32_16x16x32_bf16 v[102:105], v[150:153], v[182:185], 0
	v_mfma_f32_16x16x32_bf16 v[92:95], v[142:145], v[190:193], 0
	v_mfma_f32_16x16x32_bf16 v[84:87], v[150:153], v[190:193], 0
	v_mfma_f32_16x16x32_bf16 v[76:79], v[142:145], v[198:201], 0
	v_mfma_f32_16x16x32_bf16 v[68:71], v[150:153], v[198:201], 0
	v_mfma_f32_16x16x32_bf16 v[126:129], v[146:149], v[178:181], v[126:129]
	v_mfma_f32_16x16x32_bf16 v[118:121], v[154:157], v[178:181], v[118:121]
	v_mfma_f32_16x16x32_bf16 v[110:113], v[146:149], v[186:189], v[110:113]
	v_mfma_f32_16x16x32_bf16 v[102:105], v[154:157], v[186:189], v[102:105]
	v_mfma_f32_16x16x32_bf16 v[92:95], v[146:149], v[194:197], v[92:95]
	v_mfma_f32_16x16x32_bf16 v[84:87], v[154:157], v[194:197], v[84:87]
	v_mfma_f32_16x16x32_bf16 v[76:79], v[146:149], v[202:205], v[76:79]
	v_mfma_f32_16x16x32_bf16 v[68:71], v[154:157], v[202:205], v[68:71]
	s_setprio 0
	s_setprio 1
	v_mfma_f32_16x16x32_bf16 v[122:125], v[158:161], v[174:177], 0
	v_mfma_f32_16x16x32_bf16 v[114:117], v[166:169], v[174:177], 0
	v_mfma_f32_16x16x32_bf16 v[106:109], v[158:161], v[182:185], 0
	v_mfma_f32_16x16x32_bf16 v[98:101], v[166:169], v[182:185], 0
	v_mfma_f32_16x16x32_bf16 v[88:91], v[158:161], v[190:193], 0
	v_mfma_f32_16x16x32_bf16 v[80:83], v[166:169], v[190:193], 0
	v_mfma_f32_16x16x32_bf16 v[72:75], v[158:161], v[198:201], 0
	v_mfma_f32_16x16x32_bf16 v[64:67], v[166:169], v[198:201], 0
	v_mfma_f32_16x16x32_bf16 v[122:125], v[162:165], v[178:181], v[122:125]
	v_mfma_f32_16x16x32_bf16 v[114:117], v[170:173], v[178:181], v[114:117]
	v_mfma_f32_16x16x32_bf16 v[106:109], v[162:165], v[186:189], v[106:109]
	v_mfma_f32_16x16x32_bf16 v[98:101], v[170:173], v[186:189], v[98:101]
	v_mfma_f32_16x16x32_bf16 v[88:91], v[162:165], v[194:197], v[88:91]
	v_mfma_f32_16x16x32_bf16 v[80:83], v[170:173], v[194:197], v[80:83]
	v_mfma_f32_16x16x32_bf16 v[72:75], v[162:165], v[202:205], v[72:75]
	v_mfma_f32_16x16x32_bf16 v[64:67], v[170:173], v[202:205], v[64:67]
	s_setprio 0
	s_barrier
	v_mov_b32_e32 v96, v134
	s_add_i32 s76, s76, s25
	ds_read_b128 v[174:177], v140 offset:16384
	ds_read_b128 v[178:181], v140 offset:17408
	ds_read_b128 v[182:185], v140 offset:18432
	ds_read_b128 v[186:189], v140 offset:19456
	ds_read_b128 v[190:193], v140 offset:20480
	ds_read_b128 v[194:197], v140 offset:21504
	ds_read_b128 v[198:201], v140 offset:22528
	ds_read_b128 v[202:205], v140 offset:23552
	s_mov_b32 m0, s76
	s_nop 0
	global_load_lds_dwordx4 v96, s[22:23]
	v_mov_b32_e32 v96, v136
	s_add_i32 m0, s76, 0x2000
	s_add_u32 s78, s22, 0x80000
	global_load_lds_dwordx4 v96, s[22:23]
	s_addc_u32 s79, s23, 0
	v_mov_b32_e32 v96, v134
	s_add_i32 s76, s80, s25
	s_mov_b32 m0, s76
	s_nop 0
	global_load_lds_dwordx4 v96, s[78:79]
	v_mov_b32_e32 v96, v136
	s_add_i32 m0, s76, 0x2000
	s_nop 0
	global_load_lds_dwordx4 v96, s[78:79]
	v_mov_b32_e32 v96, v131
	s_mov_b32 m0, s26
	s_nop 0
	global_load_lds_dwordx4 v96, s[20:21]
	v_mov_b32_e32 v96, v135
	s_mov_b32 m0, s27
	s_nop 0
	global_load_lds_dwordx4 v96, s[20:21]
	s_waitcnt vmcnt(8)
	s_waitcnt lgkmcnt(0)
	s_barrier
	s_setprio 1
	s_waitcnt lgkmcnt(0)
	v_mfma_f32_16x16x32_bf16 v[60:63], v[142:145], v[174:177], 0
	v_mfma_f32_16x16x32_bf16 v[52:55], v[150:153], v[174:177], 0
	v_mfma_f32_16x16x32_bf16 v[44:47], v[142:145], v[182:185], 0
	v_mfma_f32_16x16x32_bf16 v[36:39], v[150:153], v[182:185], 0
	v_mfma_f32_16x16x32_bf16 v[28:31], v[142:145], v[190:193], 0
	v_mfma_f32_16x16x32_bf16 v[20:23], v[150:153], v[190:193], 0
	v_mfma_f32_16x16x32_bf16 v[12:15], v[142:145], v[198:201], 0
	v_mfma_f32_16x16x32_bf16 v[4:7], v[150:153], v[198:201], 0
	v_mfma_f32_16x16x32_bf16 v[60:63], v[146:149], v[178:181], v[60:63]
	v_mfma_f32_16x16x32_bf16 v[52:55], v[154:157], v[178:181], v[52:55]
	v_mfma_f32_16x16x32_bf16 v[44:47], v[146:149], v[186:189], v[44:47]
	v_mfma_f32_16x16x32_bf16 v[36:39], v[154:157], v[186:189], v[36:39]
	v_mfma_f32_16x16x32_bf16 v[28:31], v[146:149], v[194:197], v[28:31]
	v_mfma_f32_16x16x32_bf16 v[20:23], v[154:157], v[194:197], v[20:23]
	v_mfma_f32_16x16x32_bf16 v[12:15], v[146:149], v[202:205], v[12:15]
	v_mfma_f32_16x16x32_bf16 v[4:7], v[154:157], v[202:205], v[4:7]
	s_setprio 0
	s_setprio 1
	v_mfma_f32_16x16x32_bf16 v[56:59], v[158:161], v[174:177], 0
	v_mfma_f32_16x16x32_bf16 v[48:51], v[166:169], v[174:177], 0
	v_mfma_f32_16x16x32_bf16 v[40:43], v[158:161], v[182:185], 0
	v_mfma_f32_16x16x32_bf16 v[32:35], v[166:169], v[182:185], 0
	v_mfma_f32_16x16x32_bf16 v[24:27], v[158:161], v[190:193], 0
	v_mfma_f32_16x16x32_bf16 v[16:19], v[166:169], v[190:193], 0
	v_mfma_f32_16x16x32_bf16 v[8:11], v[158:161], v[198:201], 0
	v_mfma_f32_16x16x32_bf16 v[0:3], v[166:169], v[198:201], 0
	v_mfma_f32_16x16x32_bf16 v[56:59], v[162:165], v[178:181], v[56:59]
	v_mfma_f32_16x16x32_bf16 v[48:51], v[170:173], v[178:181], v[48:51]
	v_mfma_f32_16x16x32_bf16 v[40:43], v[162:165], v[186:189], v[40:43]
	v_mfma_f32_16x16x32_bf16 v[32:35], v[170:173], v[186:189], v[32:35]
	v_mfma_f32_16x16x32_bf16 v[24:27], v[162:165], v[194:197], v[24:27]
	v_mfma_f32_16x16x32_bf16 v[16:19], v[170:173], v[194:197], v[16:19]
	v_mfma_f32_16x16x32_bf16 v[8:11], v[162:165], v[202:205], v[8:11]
	v_mfma_f32_16x16x32_bf16 v[0:3], v[170:173], v[202:205], v[0:3]
	s_setprio 0
	s_barrier
	s_add_i32 s76, 0, 0x18000
	v_add_u32_e32 v96, s76, v138
	s_add_i32 s80, 0, 0x1c000
	ds_read_b128 v[142:145], v96
	ds_read_b128 v[146:149], v96 offset:1024
	ds_read_b128 v[150:153], v96 offset:2048
	ds_read_b128 v[154:157], v96 offset:3072
	v_add_u32_e32 v96, s80, v138
	ds_read_b128 v[158:161], v96
	ds_read_b128 v[162:165], v96 offset:1024
	ds_read_b128 v[166:169], v96 offset:2048
	ds_read_b128 v[170:173], v96 offset:3072
	s_add_u32 s78, s20, 0x80000
	v_mov_b32_e32 v96, v131
	s_mov_b32 m0, s28
	ds_read_b128 v[174:177], v140 offset:32768
	ds_read_b128 v[178:181], v140 offset:33792
	ds_read_b128 v[182:185], v140 offset:34816
	ds_read_b128 v[186:189], v140 offset:35840
	ds_read_b128 v[190:193], v140 offset:36864
	ds_read_b128 v[194:197], v140 offset:37888
	ds_read_b128 v[198:201], v140 offset:38912
	ds_read_b128 v[202:205], v140 offset:39936
	s_addc_u32 s79, s21, 0
	s_nop 0
	global_load_lds_dwordx4 v96, s[78:79]
	v_mov_b32_e32 v96, v135
	s_mov_b32 m0, s29
	s_nop 0
	global_load_lds_dwordx4 v96, s[78:79]
	s_waitcnt vmcnt(8)
	s_waitcnt lgkmcnt(0)
	s_barrier
	s_setprio 1
	s_waitcnt lgkmcnt(0)
	v_mfma_f32_16x16x32_bf16 v[126:129], v[142:145], v[174:177], v[126:129]
	v_mfma_f32_16x16x32_bf16 v[118:121], v[150:153], v[174:177], v[118:121]
	v_mfma_f32_16x16x32_bf16 v[110:113], v[142:145], v[182:185], v[110:113]
	v_mfma_f32_16x16x32_bf16 v[102:105], v[150:153], v[182:185], v[102:105]
	v_mfma_f32_16x16x32_bf16 v[92:95], v[142:145], v[190:193], v[92:95]
	v_mfma_f32_16x16x32_bf16 v[84:87], v[150:153], v[190:193], v[84:87]
	v_mfma_f32_16x16x32_bf16 v[76:79], v[142:145], v[198:201], v[76:79]
	v_mfma_f32_16x16x32_bf16 v[68:71], v[150:153], v[198:201], v[68:71]
	v_mfma_f32_16x16x32_bf16 v[126:129], v[146:149], v[178:181], v[126:129]
	v_mfma_f32_16x16x32_bf16 v[118:121], v[154:157], v[178:181], v[118:121]
	v_mfma_f32_16x16x32_bf16 v[110:113], v[146:149], v[186:189], v[110:113]
	v_mfma_f32_16x16x32_bf16 v[102:105], v[154:157], v[186:189], v[102:105]
	v_mfma_f32_16x16x32_bf16 v[92:95], v[146:149], v[194:197], v[92:95]
	v_mfma_f32_16x16x32_bf16 v[84:87], v[154:157], v[194:197], v[84:87]
	v_mfma_f32_16x16x32_bf16 v[76:79], v[146:149], v[202:205], v[76:79]
	v_mfma_f32_16x16x32_bf16 v[68:71], v[154:157], v[202:205], v[68:71]
	s_setprio 0
	s_setprio 1
	v_mfma_f32_16x16x32_bf16 v[122:125], v[158:161], v[174:177], v[122:125]
	v_mfma_f32_16x16x32_bf16 v[114:117], v[166:169], v[174:177], v[114:117]
	v_mfma_f32_16x16x32_bf16 v[106:109], v[158:161], v[182:185], v[106:109]
	v_mfma_f32_16x16x32_bf16 v[98:101], v[166:169], v[182:185], v[98:101]
	v_mfma_f32_16x16x32_bf16 v[88:91], v[158:161], v[190:193], v[88:91]
	v_mfma_f32_16x16x32_bf16 v[80:83], v[166:169], v[190:193], v[80:83]
	v_mfma_f32_16x16x32_bf16 v[72:75], v[158:161], v[198:201], v[72:75]
	v_mfma_f32_16x16x32_bf16 v[64:67], v[166:169], v[198:201], v[64:67]
	v_mfma_f32_16x16x32_bf16 v[122:125], v[162:165], v[178:181], v[122:125]
	v_mfma_f32_16x16x32_bf16 v[114:117], v[170:173], v[178:181], v[114:117]
	v_mfma_f32_16x16x32_bf16 v[106:109], v[162:165], v[186:189], v[106:109]
	v_mfma_f32_16x16x32_bf16 v[98:101], v[170:173], v[186:189], v[98:101]
	v_mfma_f32_16x16x32_bf16 v[88:91], v[162:165], v[194:197], v[88:91]
	v_mfma_f32_16x16x32_bf16 v[80:83], v[170:173], v[194:197], v[80:83]
	v_mfma_f32_16x16x32_bf16 v[72:75], v[162:165], v[202:205], v[72:75]
	v_mfma_f32_16x16x32_bf16 v[64:67], v[170:173], v[202:205], v[64:67]
	s_setprio 0
	s_barrier
	v_mov_b32_e32 v96, v134
	ds_read_b128 v[174:177], v140 offset:49152
	ds_read_b128 v[178:181], v140 offset:50176
	ds_read_b128 v[182:185], v140 offset:51200
	ds_read_b128 v[186:189], v140 offset:52224
	ds_read_b128 v[190:193], v140 offset:53248
	ds_read_b128 v[194:197], v140 offset:54272
	ds_read_b128 v[198:201], v140 offset:55296
	ds_read_b128 v[202:205], v140 offset:56320
	s_add_i32 s76, s76, s25
	v_lshl_add_u64 v[132:133], s[22:23], 0, v[96:97]
	v_lshl_add_u64 v[132:133], v[132:133], 0, s[0:1]
	s_mov_b32 m0, s76
	v_mov_b32_e32 v96, v136
	global_load_lds_dwordx4 v[132:133], off
	s_add_i32 m0, s76, 0x2000
	s_nop 0
	v_lshl_add_u64 v[132:133], s[22:23], 0, v[96:97]
	s_add_u32 s22, s22, 0x80080
	v_lshl_add_u64 v[132:133], v[132:133], 0, s[0:1]
	s_addc_u32 s23, s23, 0
	v_mov_b32_e32 v96, v134
	s_add_i32 s76, s80, s25
	global_load_lds_dwordx4 v[132:133], off
	s_mov_b32 m0, s76
	s_nop 0
	global_load_lds_dwordx4 v96, s[22:23]
	v_mov_b32_e32 v96, v136
	s_add_i32 m0, s76, 0x2000
	s_nop 0
	global_load_lds_dwordx4 v96, s[22:23]
	v_mov_b32_e32 v96, v131
	s_mov_b32 m0, s31
	v_lshl_add_u64 v[132:133], s[20:21], 0, v[96:97]
	v_lshl_add_u64 v[132:133], v[132:133], 0, s[0:1]
	v_mov_b32_e32 v96, v135
	global_load_lds_dwordx4 v[132:133], off
	s_mov_b32 m0, s35
	v_lshl_add_u64 v[132:133], s[20:21], 0, v[96:97]
	v_lshl_add_u64 v[132:133], v[132:133], 0, s[0:1]
	global_load_lds_dwordx4 v[132:133], off
	s_waitcnt vmcnt(8)
	s_waitcnt lgkmcnt(0)
	s_barrier
	s_setprio 1
	s_waitcnt lgkmcnt(0)
	v_mfma_f32_16x16x32_bf16 v[60:63], v[142:145], v[174:177], v[60:63]
	v_mfma_f32_16x16x32_bf16 v[52:55], v[150:153], v[174:177], v[52:55]
	v_mfma_f32_16x16x32_bf16 v[44:47], v[142:145], v[182:185], v[44:47]
	v_mfma_f32_16x16x32_bf16 v[36:39], v[150:153], v[182:185], v[36:39]
	v_mfma_f32_16x16x32_bf16 v[28:31], v[142:145], v[190:193], v[28:31]
	v_mfma_f32_16x16x32_bf16 v[20:23], v[150:153], v[190:193], v[20:23]
	v_mfma_f32_16x16x32_bf16 v[12:15], v[142:145], v[198:201], v[12:15]
	v_mfma_f32_16x16x32_bf16 v[4:7], v[150:153], v[198:201], v[4:7]
	v_mfma_f32_16x16x32_bf16 v[60:63], v[146:149], v[178:181], v[60:63]
	v_mfma_f32_16x16x32_bf16 v[52:55], v[154:157], v[178:181], v[52:55]
	v_mfma_f32_16x16x32_bf16 v[44:47], v[146:149], v[186:189], v[44:47]
	v_mfma_f32_16x16x32_bf16 v[36:39], v[154:157], v[186:189], v[36:39]
	v_mfma_f32_16x16x32_bf16 v[28:31], v[146:149], v[194:197], v[28:31]
	v_mfma_f32_16x16x32_bf16 v[20:23], v[154:157], v[194:197], v[20:23]
	v_mfma_f32_16x16x32_bf16 v[12:15], v[146:149], v[202:205], v[12:15]
	v_mfma_f32_16x16x32_bf16 v[4:7], v[154:157], v[202:205], v[4:7]
	s_setprio 0
	s_setprio 1
	v_mfma_f32_16x16x32_bf16 v[56:59], v[158:161], v[174:177], v[56:59]
	v_mfma_f32_16x16x32_bf16 v[48:51], v[166:169], v[174:177], v[48:51]
	v_mfma_f32_16x16x32_bf16 v[40:43], v[158:161], v[182:185], v[40:43]
	v_mfma_f32_16x16x32_bf16 v[32:35], v[166:169], v[182:185], v[32:35]
	v_mfma_f32_16x16x32_bf16 v[24:27], v[158:161], v[190:193], v[24:27]
	v_mfma_f32_16x16x32_bf16 v[16:19], v[166:169], v[190:193], v[16:19]
	v_mfma_f32_16x16x32_bf16 v[8:11], v[158:161], v[198:201], v[8:11]
	v_mfma_f32_16x16x32_bf16 v[0:3], v[166:169], v[198:201], v[0:3]
	v_mfma_f32_16x16x32_bf16 v[56:59], v[162:165], v[178:181], v[56:59]
	v_mfma_f32_16x16x32_bf16 v[48:51], v[170:173], v[178:181], v[48:51]
	v_mfma_f32_16x16x32_bf16 v[40:43], v[162:165], v[186:189], v[40:43]
	v_mfma_f32_16x16x32_bf16 v[32:35], v[170:173], v[186:189], v[32:35]
	v_mfma_f32_16x16x32_bf16 v[24:27], v[162:165], v[194:197], v[24:27]
	v_mfma_f32_16x16x32_bf16 v[16:19], v[170:173], v[194:197], v[16:19]
	v_mfma_f32_16x16x32_bf16 v[8:11], v[162:165], v[202:205], v[8:11]
	v_mfma_f32_16x16x32_bf16 v[0:3], v[170:173], v[202:205], v[0:3]
	s_setprio 0
	s_barrier
	s_add_i32 s47, s47, 2
	s_add_u32 s43, s43, 0x100
	s_addc_u32 s46, s46, 0
	s_add_u32 s18, s18, 0x100
	s_addc_u32 s19, s19, 0
	s_cmp_gt_u32 s47, 29
	s_cbranch_scc1 .Lmy_peel1783_exit

.LBB0_1955:
	s_add_u32 s76, s24, 0x100
	s_addc_u32 s78, s25, 0
	s_add_u32 s22, s22, 0xb0080
	s_addc_u32 s23, s23, 0
	s_mov_b32 s79, -2
	s_add_u32 s24, s22, 0xfff50080
	s_addc_u32 s25, s23, -1
	s_add_i32 s80, 0, 0x10000
	s_cmp_eq_u32 s79, 40
	s_cselect_b32 s25, s19, s25
	s_cselect_b32 s24, s18, s24
	v_add_u32_e32 v96, s80, v156
	s_cselect_b32 s27, s21, s78
	s_cselect_b32 s26, s20, s76
	s_add_i32 s82, 0, 0x14000
	ds_read_b128 v[132:135], v96
	ds_read_b128 v[136:139], v96 offset:1024
	ds_read_b128 v[140:143], v96 offset:2048
	ds_read_b128 v[144:147], v96 offset:3072
	v_add_u32_e32 v96, s82, v156
	ds_read_b128 v[160:163], v96
	ds_read_b128 v[164:167], v96 offset:1024
	ds_read_b128 v[168:171], v96 offset:2048
	ds_read_b128 v[172:175], v96 offset:3072
	v_mov_b32_e32 v96, v131
	ds_read_b128 v[176:179], v158
	ds_read_b128 v[180:183], v158 offset:1024
	ds_read_b128 v[184:187], v158 offset:2048
	ds_read_b128 v[188:191], v158 offset:3072
	ds_read_b128 v[192:195], v158 offset:4096
	ds_read_b128 v[196:199], v158 offset:5120
	ds_read_b128 v[222:225], v158 offset:6144
	ds_read_b128 v[226:229], v158 offset:7168
	s_add_i32 m0, s30, 0xc000
	s_nop 0
	global_load_lds_dwordx4 v96, s[22:23]
	v_mov_b32_e32 v96, v154
	s_add_i32 m0, s30, 0xe000
	s_nop 0
	global_load_lds_dwordx4 v96, s[22:23]
	s_waitcnt vmcnt(8)
	s_waitcnt lgkmcnt(0)
	s_barrier
	s_setprio 1
	s_waitcnt lgkmcnt(0)
	v_mfma_f32_16x16x128_f8f6f4 v[126:129], v[132:139], v[176:183], 0
	v_mfma_f32_16x16x128_f8f6f4 v[122:125], v[140:147], v[176:183], 0
	v_mfma_f32_16x16x128_f8f6f4 v[110:113], v[132:139], v[184:191], 0
	v_mfma_f32_16x16x128_f8f6f4 v[106:109], v[140:147], v[184:191], 0
	v_mfma_f32_16x16x128_f8f6f4 v[148:151], v[132:139], v[192:199], 0
	v_mfma_f32_16x16x128_f8f6f4 v[200:203], v[140:147], v[192:199], 0
	v_mfma_f32_16x16x128_f8f6f4 v[204:207], v[132:139], v[222:229], 0
	v_mfma_f32_16x16x128_f8f6f4 v[208:211], v[140:147], v[222:229], 0
	s_setprio 0
	s_setprio 1
	v_mfma_f32_16x16x128_f8f6f4 v[118:121], v[160:167], v[176:183], 0
	v_mfma_f32_16x16x128_f8f6f4 v[114:117], v[168:175], v[176:183], 0
	v_mfma_f32_16x16x128_f8f6f4 v[102:105], v[160:167], v[184:191], 0
	v_mfma_f32_16x16x128_f8f6f4 v[98:101], v[168:175], v[184:191], 0
	v_mfma_f32_16x16x128_f8f6f4 v[176:179], v[160:167], v[192:199], 0
	v_mfma_f32_16x16x128_f8f6f4 v[180:183], v[168:175], v[192:199], 0
	v_mfma_f32_16x16x128_f8f6f4 v[184:187], v[160:167], v[222:229], 0
	v_mfma_f32_16x16x128_f8f6f4 v[188:191], v[168:175], v[222:229], 0
	s_setprio 0
	s_barrier
	v_mov_b32_e32 v96, v131
	s_add_i32 s80, s80, s29
	s_nop 2
	ds_read_b128 v[64:67], v158 offset:16384
	ds_read_b128 v[68:71], v158 offset:17408
	ds_read_b128 v[72:75], v158 offset:18432
	ds_read_b128 v[76:79], v158 offset:19456
	ds_read_b128 v[80:83], v158 offset:20480
	ds_read_b128 v[84:87], v158 offset:21504
	ds_read_b128 v[88:91], v158 offset:22528
	ds_read_b128 v[92:95], v158 offset:23552
	s_mov_b32 m0, s80
	s_nop 0
	global_load_lds_dwordx4 v96, s[26:27]
	v_mov_b32_e32 v96, v154
	s_add_i32 m0, s80, 0x2000
	s_add_u32 s80, s26, 0xb0000
	global_load_lds_dwordx4 v96, s[26:27]
	s_addc_u32 s81, s27, 0
	v_mov_b32_e32 v96, v131
	s_add_i32 s82, s82, s29
	s_mov_b32 m0, s82
	s_nop 0
	global_load_lds_dwordx4 v96, s[80:81]
	v_mov_b32_e32 v96, v154
	s_add_i32 m0, s82, 0x2000
	s_nop 0
	global_load_lds_dwordx4 v96, s[80:81]
	v_mov_b32_e32 v96, v131
	s_mov_b32 m0, s30
	s_nop 0
	global_load_lds_dwordx4 v96, s[24:25]
	v_mov_b32_e32 v96, v154
	s_mov_b32 m0, s31
	s_nop 0
	global_load_lds_dwordx4 v96, s[24:25]
	s_waitcnt vmcnt(8)
	s_waitcnt lgkmcnt(0)
	s_barrier
	s_setprio 1
	s_waitcnt lgkmcnt(0)
	v_mfma_f32_16x16x128_f8f6f4 v[60:63], v[132:139], v[64:71], 0
	v_mfma_f32_16x16x128_f8f6f4 v[56:59], v[140:147], v[64:71], 0
	v_mfma_f32_16x16x128_f8f6f4 v[192:195], v[132:139], v[72:79], 0
	v_mfma_f32_16x16x128_f8f6f4 v[196:199], v[140:147], v[72:79], 0
	v_mfma_f32_16x16x128_f8f6f4 v[212:215], v[132:139], v[80:87], 0
	v_mfma_f32_16x16x128_f8f6f4 v[218:221], v[140:147], v[80:87], 0
	v_mfma_f32_16x16x128_f8f6f4 v[222:225], v[132:139], v[88:95], 0
	v_mfma_f32_16x16x128_f8f6f4 v[226:229], v[140:147], v[88:95], 0
	s_setprio 0
	s_setprio 1
	v_mfma_f32_16x16x128_f8f6f4 v[52:55], v[160:167], v[64:71], 0
	v_mfma_f32_16x16x128_f8f6f4 v[48:51], v[168:175], v[64:71], 0
	v_mfma_f32_16x16x128_f8f6f4 v[230:233], v[160:167], v[72:79], 0
	v_mfma_f32_16x16x128_f8f6f4 v[234:237], v[168:175], v[72:79], 0
	v_mfma_f32_16x16x128_f8f6f4 v[238:241], v[160:167], v[80:87], 0
	v_mfma_f32_16x16x128_f8f6f4 v[242:245], v[168:175], v[80:87], 0
	v_mfma_f32_16x16x128_f8f6f4 v[246:249], v[160:167], v[88:95], 0
	v_mfma_f32_16x16x128_f8f6f4 v[250:253], v[168:175], v[88:95], 0
	s_setprio 0
	s_barrier
	s_add_i32 s82, 0, 0x18000
	v_add_u32_e32 v8, s82, v156
	s_add_i32 s83, 0, 0x1c000
	s_nop 1
	ds_read_b128 v[0:3], v8
	ds_read_b128 v[4:7], v8 offset:1024
	ds_read_b128 v[16:19], v8 offset:2048
	ds_read_b128 v[20:23], v8 offset:3072
	v_add_u32_e32 v8, s83, v156
	ds_read_b128 v[132:135], v8
	ds_read_b128 v[136:139], v8 offset:1024
	ds_read_b128 v[140:143], v8 offset:2048
	ds_read_b128 v[144:147], v8 offset:3072
	s_add_u32 s80, s24, 0xb0000
	v_mov_b32_e32 v64, v131
	s_mov_b32 m0, s35
	ds_read_b128 v[8:11], v158 offset:32768
	ds_read_b128 v[12:15], v158 offset:33792
	ds_read_b128 v[24:27], v158 offset:34816
	ds_read_b128 v[28:31], v158 offset:35840
	ds_read_b128 v[32:35], v158 offset:36864
	ds_read_b128 v[36:39], v158 offset:37888
	ds_read_b128 v[40:43], v158 offset:38912
	ds_read_b128 v[44:47], v158 offset:39936
	s_addc_u32 s81, s25, 0
	s_nop 0
	global_load_lds_dwordx4 v64, s[80:81]
	v_mov_b32_e32 v64, v154
	s_mov_b32 m0, s36
	s_nop 0
	global_load_lds_dwordx4 v64, s[80:81]
	s_waitcnt vmcnt(8)
	s_waitcnt lgkmcnt(0)
	s_barrier
	s_setprio 1
	s_waitcnt lgkmcnt(0)
	v_mfma_f32_16x16x128_f8f6f4 v[126:129], v[0:7], v[8:15], v[126:129]
	v_mfma_f32_16x16x128_f8f6f4 v[122:125], v[16:23], v[8:15], v[122:125]
	v_mfma_f32_16x16x128_f8f6f4 v[110:113], v[0:7], v[24:31], v[110:113]
	v_mfma_f32_16x16x128_f8f6f4 v[106:109], v[16:23], v[24:31], v[106:109]
	v_mfma_f32_16x16x128_f8f6f4 v[92:95], v[0:7], v[32:39], v[148:151]
	v_mfma_f32_16x16x128_f8f6f4 v[88:91], v[16:23], v[32:39], v[200:203]
	v_mfma_f32_16x16x128_f8f6f4 v[76:79], v[0:7], v[40:47], v[204:207]
	v_mfma_f32_16x16x128_f8f6f4 v[72:75], v[16:23], v[40:47], v[208:211]
	s_setprio 0
	s_setprio 1
	v_mfma_f32_16x16x128_f8f6f4 v[118:121], v[132:139], v[8:15], v[118:121]
	v_mfma_f32_16x16x128_f8f6f4 v[114:117], v[140:147], v[8:15], v[114:117]
	v_mfma_f32_16x16x128_f8f6f4 v[102:105], v[132:139], v[24:31], v[102:105]
	v_mfma_f32_16x16x128_f8f6f4 v[98:101], v[140:147], v[24:31], v[98:101]
	v_mfma_f32_16x16x128_f8f6f4 v[84:87], v[132:139], v[32:39], v[176:179]
	v_mfma_f32_16x16x128_f8f6f4 v[80:83], v[140:147], v[32:39], v[180:183]
	v_mfma_f32_16x16x128_f8f6f4 v[68:71], v[132:139], v[40:47], v[184:187]
	v_mfma_f32_16x16x128_f8f6f4 v[64:67], v[140:147], v[40:47], v[188:191]
	s_setprio 0
	s_barrier
	v_mov_b32_e32 v96, v131
	ds_read_b128 v[32:35], v158 offset:49152
	ds_read_b128 v[36:39], v158 offset:50176
	ds_read_b128 v[160:163], v158 offset:51200
	ds_read_b128 v[164:167], v158 offset:52224
	ds_read_b128 v[168:171], v158 offset:53248
	ds_read_b128 v[172:175], v158 offset:54272
	ds_read_b128 v[176:179], v158 offset:55296
	ds_read_b128 v[180:183], v158 offset:56320
	s_add_i32 s80, s82, s29
	v_lshl_add_u64 v[8:9], s[26:27], 0, v[96:97]
	v_lshl_add_u64 v[8:9], v[8:9], 0, s[0:1]
	s_mov_b32 m0, s80
	v_mov_b32_e32 v96, v154
	global_load_lds_dwordx4 v[8:9], off
	s_add_i32 m0, s80, 0x2000
	v_lshl_add_u64 v[8:9], s[26:27], 0, v[96:97]
	v_lshl_add_u64 v[8:9], v[8:9], 0, s[0:1]
	s_add_u32 s26, s26, 0xb0080
	global_load_lds_dwordx4 v[8:9], off
	s_addc_u32 s27, s27, 0
	v_mov_b32_e32 v8, v131
	s_add_i32 s80, s83, s29
	s_mov_b32 m0, s80
	v_mov_b32_e32 v96, v131
	global_load_lds_dwordx4 v8, s[26:27]
	v_mov_b32_e32 v8, v154
	s_add_i32 m0, s80, 0x2000
	s_nop 0
	global_load_lds_dwordx4 v8, s[26:27]
	s_mov_b32 m0, s37
	v_lshl_add_u64 v[8:9], s[24:25], 0, v[96:97]
	v_lshl_add_u64 v[8:9], v[8:9], 0, s[0:1]
	v_mov_b32_e32 v96, v154
	global_load_lds_dwordx4 v[8:9], off
	s_mov_b32 m0, s38
	v_lshl_add_u64 v[8:9], s[24:25], 0, v[96:97]
	v_lshl_add_u64 v[8:9], v[8:9], 0, s[0:1]
	global_load_lds_dwordx4 v[8:9], off
	s_waitcnt vmcnt(8)
	s_waitcnt lgkmcnt(0)
	s_barrier
	s_setprio 1
	s_waitcnt lgkmcnt(0)
	v_mfma_f32_16x16x128_f8f6f4 v[60:63], v[0:7], v[32:39], v[60:63]
	v_mfma_f32_16x16x128_f8f6f4 v[56:59], v[16:23], v[32:39], v[56:59]
	v_mfma_f32_16x16x128_f8f6f4 v[44:47], v[0:7], v[160:167], v[192:195]
	v_mfma_f32_16x16x128_f8f6f4 v[40:43], v[16:23], v[160:167], v[196:199]
	v_mfma_f32_16x16x128_f8f6f4 v[28:31], v[0:7], v[168:175], v[212:215]
	v_mfma_f32_16x16x128_f8f6f4 v[24:27], v[16:23], v[168:175], v[218:221]
	v_mfma_f32_16x16x128_f8f6f4 v[12:15], v[0:7], v[176:183], v[222:225]
	v_mfma_f32_16x16x128_f8f6f4 v[8:11], v[16:23], v[176:183], v[226:229]
	s_setprio 0
	s_setprio 1
	v_mfma_f32_16x16x128_f8f6f4 v[52:55], v[132:139], v[32:39], v[52:55]
	v_mfma_f32_16x16x128_f8f6f4 v[48:51], v[140:147], v[32:39], v[48:51]
	v_mfma_f32_16x16x128_f8f6f4 v[36:39], v[132:139], v[160:167], v[230:233]
	v_mfma_f32_16x16x128_f8f6f4 v[32:35], v[140:147], v[160:167], v[234:237]
	v_mfma_f32_16x16x128_f8f6f4 v[20:23], v[132:139], v[168:175], v[238:241]
	v_mfma_f32_16x16x128_f8f6f4 v[16:19], v[140:147], v[168:175], v[242:245]
	v_mfma_f32_16x16x128_f8f6f4 v[4:7], v[132:139], v[176:183], v[246:249]
	v_mfma_f32_16x16x128_f8f6f4 v[0:3], v[140:147], v[176:183], v[250:253]
	s_setprio 0
	s_barrier
	s_add_i32 s79, s79, 2
	s_add_u32 s76, s76, 0x100
	s_addc_u32 s78, s78, 0
	s_add_u32 s22, s22, 0x100
	s_addc_u32 s23, s23, 0
	s_cmp_gt_u32 s79, 41
	s_cbranch_scc1 .Lmy_peel1956_exit

.Lmy_peel1956_exit:
	s_and_b64 vcc, exec, s[10:11]
	s_cbranch_vccz .LBB0_1959
	s_barrier

.LBB0_2128:
	s_add_u32 s39, s18, 0x100
	s_addc_u32 s40, s19, 0
	s_add_u32 s16, s16, 0x40080
	s_addc_u32 s17, s17, 0
	s_mov_b32 s41, -2
	s_add_u32 s18, s16, 0xfffc0080
	s_addc_u32 s19, s17, -1
	s_add_i32 s42, 0, 0x10000
	s_cmp_eq_u32 s41, 12
	s_cselect_b32 s19, s13, s19
	s_cselect_b32 s18, s12, s18
	v_add_u32_e32 v96, s42, v137
	s_cselect_b32 s21, s15, s40
	s_cselect_b32 s20, s14, s39
	s_add_i32 s46, 0, 0x14000
	ds_read_b128 v[140:143], v96
	ds_read_b128 v[144:147], v96 offset:1024
	ds_read_b128 v[148:151], v96 offset:2048
	ds_read_b128 v[152:155], v96 offset:3072
	v_add_u32_e32 v96, s46, v137
	ds_read_b128 v[156:159], v96
	ds_read_b128 v[160:163], v96 offset:1024
	ds_read_b128 v[164:167], v96 offset:2048
	ds_read_b128 v[168:171], v96 offset:3072
	v_mov_b32_e32 v96, v132
	ds_read_b128 v[172:175], v139
	ds_read_b128 v[176:179], v139 offset:1024
	ds_read_b128 v[180:183], v139 offset:2048
	ds_read_b128 v[184:187], v139 offset:3072
	ds_read_b128 v[188:191], v139 offset:4096
	ds_read_b128 v[192:195], v139 offset:5120
	ds_read_b128 v[196:199], v139 offset:6144
	ds_read_b128 v[200:203], v139 offset:7168
	s_add_i32 m0, s24, 0xc000
	s_nop 0
	global_load_lds_dwordx4 v96, s[16:17]
	v_mov_b32_e32 v96, v134
	s_add_i32 m0, s24, 0xe000
	s_nop 0
	global_load_lds_dwordx4 v96, s[16:17]
	s_waitcnt vmcnt(8)
	s_waitcnt lgkmcnt(0)
	s_barrier
	s_setprio 1
	s_waitcnt lgkmcnt(0)
	v_mfma_f32_16x16x128_f8f6f4 v[126:129], v[140:147], v[172:179], 0
	v_mfma_f32_16x16x128_f8f6f4 v[118:121], v[148:155], v[172:179], 0
	v_mfma_f32_16x16x128_f8f6f4 v[110:113], v[140:147], v[180:187], 0
	v_mfma_f32_16x16x128_f8f6f4 v[102:105], v[148:155], v[180:187], 0
	v_mfma_f32_16x16x128_f8f6f4 v[204:207], v[140:147], v[188:195], 0
	v_mfma_f32_16x16x128_f8f6f4 v[208:211], v[148:155], v[188:195], 0
	v_mfma_f32_16x16x128_f8f6f4 v[212:215], v[140:147], v[196:203], 0
	v_mfma_f32_16x16x128_f8f6f4 v[218:221], v[148:155], v[196:203], 0
	s_setprio 0
	s_setprio 1
	v_mfma_f32_16x16x128_f8f6f4 v[122:125], v[156:163], v[172:179], 0
	v_mfma_f32_16x16x128_f8f6f4 v[114:117], v[164:171], v[172:179], 0
	v_mfma_f32_16x16x128_f8f6f4 v[106:109], v[156:163], v[180:187], 0
	v_mfma_f32_16x16x128_f8f6f4 v[98:101], v[164:171], v[180:187], 0
	v_mfma_f32_16x16x128_f8f6f4 v[172:175], v[156:163], v[188:195], 0
	v_mfma_f32_16x16x128_f8f6f4 v[176:179], v[164:171], v[188:195], 0
	v_mfma_f32_16x16x128_f8f6f4 v[180:183], v[156:163], v[196:203], 0
	v_mfma_f32_16x16x128_f8f6f4 v[184:187], v[164:171], v[196:203], 0
	s_setprio 0
	s_barrier
	v_mov_b32_e32 v96, v133
	s_add_i32 s42, s42, s23
	s_nop 2
	ds_read_b128 v[64:67], v139 offset:16384
	ds_read_b128 v[68:71], v139 offset:17408
	ds_read_b128 v[72:75], v139 offset:18432
	ds_read_b128 v[76:79], v139 offset:19456
	ds_read_b128 v[80:83], v139 offset:20480
	ds_read_b128 v[84:87], v139 offset:21504
	ds_read_b128 v[88:91], v139 offset:22528
	ds_read_b128 v[92:95], v139 offset:23552
	s_mov_b32 m0, s42
	s_nop 0
	global_load_lds_dwordx4 v96, s[20:21]
	v_mov_b32_e32 v96, v135
	s_add_i32 m0, s42, 0x2000
	s_add_u32 s42, s20, 0x40000
	global_load_lds_dwordx4 v96, s[20:21]
	s_addc_u32 s43, s21, 0
	v_mov_b32_e32 v96, v133
	s_add_i32 s46, s46, s23
	s_mov_b32 m0, s46
	s_nop 0
	global_load_lds_dwordx4 v96, s[42:43]
	v_mov_b32_e32 v96, v135
	s_add_i32 m0, s46, 0x2000
	s_nop 0
	global_load_lds_dwordx4 v96, s[42:43]
	v_mov_b32_e32 v96, v132
	s_mov_b32 m0, s24
	s_nop 0
	global_load_lds_dwordx4 v96, s[18:19]
	v_mov_b32_e32 v96, v134
	s_mov_b32 m0, s25
	s_nop 0
	global_load_lds_dwordx4 v96, s[18:19]
	s_waitcnt vmcnt(8)
	s_waitcnt lgkmcnt(0)
	s_barrier
	s_setprio 1
	s_waitcnt lgkmcnt(0)
	v_mfma_f32_16x16x128_f8f6f4 v[60:63], v[140:147], v[64:71], 0
	v_mfma_f32_16x16x128_f8f6f4 v[52:55], v[148:155], v[64:71], 0
	v_mfma_f32_16x16x128_f8f6f4 v[44:47], v[140:147], v[72:79], 0
	v_mfma_f32_16x16x128_f8f6f4 v[196:199], v[148:155], v[72:79], 0
	v_mfma_f32_16x16x128_f8f6f4 v[200:203], v[140:147], v[80:87], 0
	v_mfma_f32_16x16x128_f8f6f4 v[222:225], v[148:155], v[80:87], 0
	v_mfma_f32_16x16x128_f8f6f4 v[226:229], v[140:147], v[88:95], 0
	v_mfma_f32_16x16x128_f8f6f4 v[230:233], v[148:155], v[88:95], 0
	s_setprio 0
	s_setprio 1
	v_mfma_f32_16x16x128_f8f6f4 v[56:59], v[156:163], v[64:71], 0
	v_mfma_f32_16x16x128_f8f6f4 v[48:51], v[164:171], v[64:71], 0
	v_mfma_f32_16x16x128_f8f6f4 v[40:43], v[156:163], v[72:79], 0
	v_mfma_f32_16x16x128_f8f6f4 v[234:237], v[164:171], v[72:79], 0
	v_mfma_f32_16x16x128_f8f6f4 v[238:241], v[156:163], v[80:87], 0
	v_mfma_f32_16x16x128_f8f6f4 v[242:245], v[164:171], v[80:87], 0
	v_mfma_f32_16x16x128_f8f6f4 v[246:249], v[156:163], v[88:95], 0
	v_mfma_f32_16x16x128_f8f6f4 v[250:253], v[164:171], v[88:95], 0
	s_setprio 0
	s_barrier
	s_add_i32 s46, 0, 0x18000
	s_nop 2
	v_add_u32_e32 v8, s46, v137
	s_add_i32 s47, 0, 0x1c000
	ds_read_b128 v[0:3], v8
	ds_read_b128 v[4:7], v8 offset:1024
	ds_read_b128 v[140:143], v8 offset:2048
	ds_read_b128 v[144:147], v8 offset:3072
	v_add_u32_e32 v8, s47, v137
	ds_read_b128 v[148:151], v8
	ds_read_b128 v[152:155], v8 offset:1024
	ds_read_b128 v[156:159], v8 offset:2048
	ds_read_b128 v[160:163], v8 offset:3072
	s_add_u32 s42, s18, 0x40000
	v_mov_b32_e32 v64, v132
	s_mov_b32 m0, s26
	ds_read_b128 v[8:11], v139 offset:32768
	ds_read_b128 v[12:15], v139 offset:33792
	ds_read_b128 v[16:19], v139 offset:34816
	ds_read_b128 v[20:23], v139 offset:35840
	ds_read_b128 v[24:27], v139 offset:36864
	ds_read_b128 v[28:31], v139 offset:37888
	ds_read_b128 v[32:35], v139 offset:38912
	ds_read_b128 v[36:39], v139 offset:39936
	s_addc_u32 s43, s19, 0
	s_nop 0
	global_load_lds_dwordx4 v64, s[42:43]
	v_mov_b32_e32 v64, v134
	s_mov_b32 m0, s27
	s_nop 0
	global_load_lds_dwordx4 v64, s[42:43]
	s_waitcnt vmcnt(8)
	s_waitcnt lgkmcnt(0)
	s_barrier
	s_setprio 1
	s_waitcnt lgkmcnt(0)
	v_mfma_f32_16x16x128_f8f6f4 v[126:129], v[0:7], v[8:15], v[126:129]
	v_mfma_f32_16x16x128_f8f6f4 v[118:121], v[140:147], v[8:15], v[118:121]
	v_mfma_f32_16x16x128_f8f6f4 v[110:113], v[0:7], v[16:23], v[110:113]
	v_mfma_f32_16x16x128_f8f6f4 v[102:105], v[140:147], v[16:23], v[102:105]
	v_mfma_f32_16x16x128_f8f6f4 v[92:95], v[0:7], v[24:31], v[204:207]
	v_mfma_f32_16x16x128_f8f6f4 v[84:87], v[140:147], v[24:31], v[208:211]
	v_mfma_f32_16x16x128_f8f6f4 v[76:79], v[0:7], v[32:39], v[212:215]
	v_mfma_f32_16x16x128_f8f6f4 v[68:71], v[140:147], v[32:39], v[218:221]
	s_setprio 0
	s_setprio 1
	v_mfma_f32_16x16x128_f8f6f4 v[122:125], v[148:155], v[8:15], v[122:125]
	v_mfma_f32_16x16x128_f8f6f4 v[114:117], v[156:163], v[8:15], v[114:117]
	v_mfma_f32_16x16x128_f8f6f4 v[106:109], v[148:155], v[16:23], v[106:109]
	v_mfma_f32_16x16x128_f8f6f4 v[98:101], v[156:163], v[16:23], v[98:101]
	v_mfma_f32_16x16x128_f8f6f4 v[88:91], v[148:155], v[24:31], v[172:175]
	v_mfma_f32_16x16x128_f8f6f4 v[80:83], v[156:163], v[24:31], v[176:179]
	v_mfma_f32_16x16x128_f8f6f4 v[72:75], v[148:155], v[32:39], v[180:183]
	v_mfma_f32_16x16x128_f8f6f4 v[64:67], v[156:163], v[32:39], v[184:187]
	s_setprio 0
	s_barrier
	v_mov_b32_e32 v96, v133
	ds_read_b128 v[164:167], v139 offset:49152
	ds_read_b128 v[168:171], v139 offset:50176
	ds_read_b128 v[172:175], v139 offset:51200
	ds_read_b128 v[176:179], v139 offset:52224
	ds_read_b128 v[180:183], v139 offset:53248
	ds_read_b128 v[184:187], v139 offset:54272
	ds_read_b128 v[188:191], v139 offset:55296
	ds_read_b128 v[192:195], v139 offset:56320
	s_add_i32 s42, s46, s23
	v_lshl_add_u64 v[8:9], s[20:21], 0, v[96:97]
	v_lshl_add_u64 v[8:9], v[8:9], 0, s[0:1]
	s_mov_b32 m0, s42
	v_mov_b32_e32 v96, v135
	global_load_lds_dwordx4 v[8:9], off
	s_add_i32 m0, s42, 0x2000
	v_lshl_add_u64 v[8:9], s[20:21], 0, v[96:97]
	v_lshl_add_u64 v[8:9], v[8:9], 0, s[0:1]
	s_add_u32 s20, s20, 0x40080
	global_load_lds_dwordx4 v[8:9], off
	s_addc_u32 s21, s21, 0
	v_mov_b32_e32 v8, v133
	s_add_i32 s42, s47, s23
	s_mov_b32 m0, s42
	v_mov_b32_e32 v96, v132
	global_load_lds_dwordx4 v8, s[20:21]
	v_mov_b32_e32 v8, v135
	s_add_i32 m0, s42, 0x2000
	s_nop 0
	global_load_lds_dwordx4 v8, s[20:21]
	s_mov_b32 m0, s28
	v_lshl_add_u64 v[8:9], s[18:19], 0, v[96:97]
	v_lshl_add_u64 v[8:9], v[8:9], 0, s[0:1]
	v_mov_b32_e32 v96, v134
	global_load_lds_dwordx4 v[8:9], off
	s_mov_b32 m0, s29
	v_lshl_add_u64 v[8:9], s[18:19], 0, v[96:97]
	v_lshl_add_u64 v[8:9], v[8:9], 0, s[0:1]
	global_load_lds_dwordx4 v[8:9], off
	s_waitcnt vmcnt(8)
	s_waitcnt lgkmcnt(0)
	s_barrier
	s_setprio 1
	s_waitcnt lgkmcnt(0)
	v_mfma_f32_16x16x128_f8f6f4 v[60:63], v[0:7], v[164:171], v[60:63]
	v_mfma_f32_16x16x128_f8f6f4 v[52:55], v[140:147], v[164:171], v[52:55]
	v_mfma_f32_16x16x128_f8f6f4 v[44:47], v[0:7], v[172:179], v[44:47]
	v_mfma_f32_16x16x128_f8f6f4 v[36:39], v[140:147], v[172:179], v[196:199]
	v_mfma_f32_16x16x128_f8f6f4 v[28:31], v[0:7], v[180:187], v[200:203]
	v_mfma_f32_16x16x128_f8f6f4 v[20:23], v[140:147], v[180:187], v[222:225]
	v_mfma_f32_16x16x128_f8f6f4 v[12:15], v[0:7], v[188:195], v[226:229]
	v_mfma_f32_16x16x128_f8f6f4 v[4:7], v[140:147], v[188:195], v[230:233]
	s_setprio 0
	s_setprio 1
	v_mfma_f32_16x16x128_f8f6f4 v[56:59], v[148:155], v[164:171], v[56:59]
	v_mfma_f32_16x16x128_f8f6f4 v[48:51], v[156:163], v[164:171], v[48:51]
	v_mfma_f32_16x16x128_f8f6f4 v[40:43], v[148:155], v[172:179], v[40:43]
	v_mfma_f32_16x16x128_f8f6f4 v[32:35], v[156:163], v[172:179], v[234:237]
	v_mfma_f32_16x16x128_f8f6f4 v[24:27], v[148:155], v[180:187], v[238:241]
	v_mfma_f32_16x16x128_f8f6f4 v[16:19], v[156:163], v[180:187], v[242:245]
	v_mfma_f32_16x16x128_f8f6f4 v[8:11], v[148:155], v[188:195], v[246:249]
	v_mfma_f32_16x16x128_f8f6f4 v[0:3], v[156:163], v[188:195], v[250:253]
	s_setprio 0
	s_barrier
	s_add_i32 s41, s41, 2
	s_add_u32 s39, s39, 0x100
	s_addc_u32 s40, s40, 0
	s_add_u32 s16, s16, 0x100
	s_addc_u32 s17, s17, 0
	s_cmp_gt_u32 s41, 13
	s_cbranch_scc1 .Lmy_peel2129_exit

.Lmy_peel2129_exit:
	s_and_b64 vcc, exec, s[6:7]
	s_cbranch_vccz .LBB0_2132
	s_barrier

.LBB0_2204:
	s_add_u32 s41, s20, 0x100
	s_addc_u32 s42, s21, 0
	s_add_u32 s18, s18, 0xb0080
	s_addc_u32 s19, s19, 0
	s_mov_b32 s43, -2
	s_add_u32 s20, s18, 0xfff50080
	s_addc_u32 s21, s19, -1
	s_add_i32 s46, 0, 0x10000
	s_cmp_eq_u32 s43, 40
	s_cselect_b32 s21, s15, s21
	s_cselect_b32 s20, s14, s20
	v_add_u32_e32 v96, s46, v137
	s_cselect_b32 s23, s17, s42
	s_cselect_b32 s22, s16, s41
	s_add_i32 s69, 0, 0x14000
	ds_read_b128 v[140:143], v96
	ds_read_b128 v[144:147], v96 offset:1024
	ds_read_b128 v[148:151], v96 offset:2048
	ds_read_b128 v[152:155], v96 offset:3072
	v_add_u32_e32 v96, s69, v137
	ds_read_b128 v[156:159], v96
	ds_read_b128 v[160:163], v96 offset:1024
	ds_read_b128 v[164:167], v96 offset:2048
	ds_read_b128 v[168:171], v96 offset:3072
	v_mov_b32_e32 v96, v130
	ds_read_b128 v[172:175], v139
	ds_read_b128 v[176:179], v139 offset:1024
	ds_read_b128 v[180:183], v139 offset:2048
	ds_read_b128 v[184:187], v139 offset:3072
	ds_read_b128 v[188:191], v139 offset:4096
	ds_read_b128 v[192:195], v139 offset:5120
	ds_read_b128 v[196:199], v139 offset:6144
	ds_read_b128 v[200:203], v139 offset:7168
	s_add_i32 m0, s26, 0xc000
	s_nop 0
	global_load_lds_dwordx4 v96, s[18:19]
	v_mov_b32_e32 v96, v132
	s_add_i32 m0, s26, 0xe000
	s_nop 0
	global_load_lds_dwordx4 v96, s[18:19]
	s_waitcnt vmcnt(8)
	s_waitcnt lgkmcnt(0)
	s_barrier
	s_setprio 1
	s_waitcnt lgkmcnt(0)
	v_mfma_f32_16x16x128_f8f6f4 v[126:129], v[140:147], v[172:179], 0
	v_mfma_f32_16x16x128_f8f6f4 v[122:125], v[148:155], v[172:179], 0
	v_mfma_f32_16x16x128_f8f6f4 v[118:121], v[140:147], v[180:187], 0
	v_mfma_f32_16x16x128_f8f6f4 v[110:113], v[148:155], v[180:187], 0
	v_mfma_f32_16x16x128_f8f6f4 v[102:105], v[140:147], v[188:195], 0
	v_mfma_f32_16x16x128_f8f6f4 v[204:207], v[148:155], v[188:195], 0
	v_mfma_f32_16x16x128_f8f6f4 v[208:211], v[140:147], v[196:203], 0
	v_mfma_f32_16x16x128_f8f6f4 v[212:215], v[148:155], v[196:203], 0
	s_setprio 0
	s_setprio 1
	v_mfma_f32_16x16x128_f8f6f4 v[114:117], v[156:163], v[172:179], 0
	v_mfma_f32_16x16x128_f8f6f4 v[106:109], v[164:171], v[172:179], 0
	v_mfma_f32_16x16x128_f8f6f4 v[98:101], v[156:163], v[180:187], 0
	v_mfma_f32_16x16x128_f8f6f4 v[172:175], v[164:171], v[180:187], 0
	v_mfma_f32_16x16x128_f8f6f4 v[176:179], v[156:163], v[188:195], 0
	v_mfma_f32_16x16x128_f8f6f4 v[180:183], v[164:171], v[188:195], 0
	v_mfma_f32_16x16x128_f8f6f4 v[184:187], v[156:163], v[196:203], 0
	v_mfma_f32_16x16x128_f8f6f4 v[188:191], v[164:171], v[196:203], 0
	s_setprio 0
	s_barrier
	v_mov_b32_e32 v96, v131
	s_add_i32 s46, s46, s25
	s_nop 2
	ds_read_b128 v[64:67], v139 offset:16384
	ds_read_b128 v[68:71], v139 offset:17408
	ds_read_b128 v[72:75], v139 offset:18432
	ds_read_b128 v[76:79], v139 offset:19456
	ds_read_b128 v[80:83], v139 offset:20480
	ds_read_b128 v[84:87], v139 offset:21504
	ds_read_b128 v[88:91], v139 offset:22528
	ds_read_b128 v[92:95], v139 offset:23552
	s_mov_b32 m0, s46
	s_nop 0
	global_load_lds_dwordx4 v96, s[22:23]
	v_mov_b32_e32 v96, v133
	s_add_i32 m0, s46, 0x2000
	s_add_u32 s46, s22, 0xb0000
	global_load_lds_dwordx4 v96, s[22:23]
	s_addc_u32 s47, s23, 0
	v_mov_b32_e32 v96, v131
	s_add_i32 s69, s69, s25
	s_mov_b32 m0, s69
	s_nop 0
	global_load_lds_dwordx4 v96, s[46:47]
	v_mov_b32_e32 v96, v133
	s_add_i32 m0, s69, 0x2000
	s_nop 0
	global_load_lds_dwordx4 v96, s[46:47]
	v_mov_b32_e32 v96, v130
	s_mov_b32 m0, s26
	s_nop 0
	global_load_lds_dwordx4 v96, s[20:21]
	v_mov_b32_e32 v96, v132
	s_mov_b32 m0, s27
	s_nop 0
	global_load_lds_dwordx4 v96, s[20:21]
	s_waitcnt vmcnt(8)
	s_waitcnt lgkmcnt(0)
	s_barrier
	s_setprio 1
	s_waitcnt lgkmcnt(0)
	v_mfma_f32_16x16x128_f8f6f4 v[60:63], v[140:147], v[64:71], 0
	v_mfma_f32_16x16x128_f8f6f4 v[56:59], v[148:155], v[64:71], 0
	v_mfma_f32_16x16x128_f8f6f4 v[52:55], v[140:147], v[72:79], 0
	v_mfma_f32_16x16x128_f8f6f4 v[192:195], v[148:155], v[72:79], 0
	v_mfma_f32_16x16x128_f8f6f4 v[196:199], v[140:147], v[80:87], 0
	v_mfma_f32_16x16x128_f8f6f4 v[200:203], v[148:155], v[80:87], 0
	v_mfma_f32_16x16x128_f8f6f4 v[218:221], v[140:147], v[88:95], 0
	v_mfma_f32_16x16x128_f8f6f4 v[222:225], v[148:155], v[88:95], 0
	s_setprio 0
	s_setprio 1
	v_mfma_f32_16x16x128_f8f6f4 v[48:51], v[156:163], v[64:71], 0
	v_mfma_f32_16x16x128_f8f6f4 v[226:229], v[164:171], v[64:71], 0
	v_mfma_f32_16x16x128_f8f6f4 v[230:233], v[156:163], v[72:79], 0
	v_mfma_f32_16x16x128_f8f6f4 v[234:237], v[164:171], v[72:79], 0
	v_mfma_f32_16x16x128_f8f6f4 v[238:241], v[156:163], v[80:87], 0
	v_mfma_f32_16x16x128_f8f6f4 v[242:245], v[164:171], v[80:87], 0
	v_mfma_f32_16x16x128_f8f6f4 v[246:249], v[156:163], v[88:95], 0
	v_mfma_f32_16x16x128_f8f6f4 v[250:253], v[164:171], v[88:95], 0
	s_setprio 0
	s_barrier
	s_add_i32 s69, 0, 0x18000
	s_add_i32 s76, 0, 0x1c000
	v_add_u32_e32 v12, s69, v137
	v_add_u32_e32 v16, s76, v137
	s_nop 0
	ds_read_b128 v[0:3], v12
	ds_read_b128 v[4:7], v12 offset:1024
	ds_read_b128 v[8:11], v12 offset:2048
	ds_read_b128 v[12:15], v12 offset:3072
	ds_read_b128 v[140:143], v16
	ds_read_b128 v[144:147], v16 offset:1024
	ds_read_b128 v[148:151], v16 offset:2048
	ds_read_b128 v[152:155], v16 offset:3072
	s_add_u32 s46, s20, 0xb0000
	v_mov_b32_e32 v64, v130
	s_mov_b32 m0, s28
	ds_read_b128 v[16:19], v139 offset:32768
	ds_read_b128 v[20:23], v139 offset:33792
	ds_read_b128 v[24:27], v139 offset:34816
	ds_read_b128 v[28:31], v139 offset:35840
	ds_read_b128 v[32:35], v139 offset:36864
	ds_read_b128 v[36:39], v139 offset:37888
	ds_read_b128 v[40:43], v139 offset:38912
	ds_read_b128 v[44:47], v139 offset:39936
	s_addc_u32 s47, s21, 0
	s_nop 0
	global_load_lds_dwordx4 v64, s[46:47]
	v_mov_b32_e32 v64, v132
	s_mov_b32 m0, s29
	s_nop 0
	global_load_lds_dwordx4 v64, s[46:47]
	s_waitcnt vmcnt(8)
	s_waitcnt lgkmcnt(0)
	s_barrier
	s_setprio 1
	s_waitcnt lgkmcnt(0)
	v_mfma_f32_16x16x128_f8f6f4 v[126:129], v[0:7], v[16:23], v[126:129]
	v_mfma_f32_16x16x128_f8f6f4 v[122:125], v[8:15], v[16:23], v[122:125]
	v_mfma_f32_16x16x128_f8f6f4 v[118:121], v[0:7], v[24:31], v[118:121]
	v_mfma_f32_16x16x128_f8f6f4 v[110:113], v[8:15], v[24:31], v[110:113]
	v_mfma_f32_16x16x128_f8f6f4 v[102:105], v[0:7], v[32:39], v[102:105]
	v_mfma_f32_16x16x128_f8f6f4 v[92:95], v[8:15], v[32:39], v[204:207]
	v_mfma_f32_16x16x128_f8f6f4 v[84:87], v[0:7], v[40:47], v[208:211]
	v_mfma_f32_16x16x128_f8f6f4 v[76:79], v[8:15], v[40:47], v[212:215]
	s_setprio 0
	s_setprio 1
	v_mfma_f32_16x16x128_f8f6f4 v[114:117], v[140:147], v[16:23], v[114:117]
	v_mfma_f32_16x16x128_f8f6f4 v[106:109], v[148:155], v[16:23], v[106:109]
	v_mfma_f32_16x16x128_f8f6f4 v[98:101], v[140:147], v[24:31], v[98:101]
	v_mfma_f32_16x16x128_f8f6f4 v[88:91], v[148:155], v[24:31], v[172:175]
	v_mfma_f32_16x16x128_f8f6f4 v[80:83], v[140:147], v[32:39], v[176:179]
	v_mfma_f32_16x16x128_f8f6f4 v[72:75], v[148:155], v[32:39], v[180:183]
	v_mfma_f32_16x16x128_f8f6f4 v[68:71], v[140:147], v[40:47], v[184:187]
	v_mfma_f32_16x16x128_f8f6f4 v[64:67], v[148:155], v[40:47], v[188:191]
	s_setprio 0
	s_barrier
	v_mov_b32_e32 v96, v131
	ds_read_b128 v[156:159], v139 offset:49152
	ds_read_b128 v[160:163], v139 offset:50176
	ds_read_b128 v[164:167], v139 offset:51200
	ds_read_b128 v[168:171], v139 offset:52224
	ds_read_b128 v[172:175], v139 offset:53248
	ds_read_b128 v[176:179], v139 offset:54272
	ds_read_b128 v[180:183], v139 offset:55296
	ds_read_b128 v[184:187], v139 offset:56320
	s_add_i32 s46, s69, s25
	v_lshl_add_u64 v[16:17], s[22:23], 0, v[96:97]
	v_lshl_add_u64 v[16:17], v[16:17], 0, s[0:1]
	s_mov_b32 m0, s46
	v_mov_b32_e32 v96, v133
	global_load_lds_dwordx4 v[16:17], off
	s_add_i32 m0, s46, 0x2000
	v_lshl_add_u64 v[16:17], s[22:23], 0, v[96:97]
	v_lshl_add_u64 v[16:17], v[16:17], 0, s[0:1]
	s_add_u32 s22, s22, 0xb0080
	global_load_lds_dwordx4 v[16:17], off
	s_addc_u32 s23, s23, 0
	v_mov_b32_e32 v16, v131
	s_add_i32 s46, s76, s25
	s_mov_b32 m0, s46
	v_mov_b32_e32 v96, v130
	global_load_lds_dwordx4 v16, s[22:23]
	v_mov_b32_e32 v16, v133
	s_add_i32 m0, s46, 0x2000
	s_nop 0
	global_load_lds_dwordx4 v16, s[22:23]
	s_mov_b32 m0, s30
	v_lshl_add_u64 v[16:17], s[20:21], 0, v[96:97]
	v_lshl_add_u64 v[16:17], v[16:17], 0, s[0:1]
	v_mov_b32_e32 v96, v132
	global_load_lds_dwordx4 v[16:17], off
	s_mov_b32 m0, s31
	v_lshl_add_u64 v[16:17], s[20:21], 0, v[96:97]
	v_lshl_add_u64 v[16:17], v[16:17], 0, s[0:1]
	global_load_lds_dwordx4 v[16:17], off
	s_waitcnt vmcnt(8)
	s_waitcnt lgkmcnt(0)
	s_barrier
	s_setprio 1
	s_waitcnt lgkmcnt(0)
	v_mfma_f32_16x16x128_f8f6f4 v[60:63], v[0:7], v[156:163], v[60:63]
	v_mfma_f32_16x16x128_f8f6f4 v[56:59], v[8:15], v[156:163], v[56:59]
	v_mfma_f32_16x16x128_f8f6f4 v[52:55], v[0:7], v[164:171], v[52:55]
	v_mfma_f32_16x16x128_f8f6f4 v[44:47], v[8:15], v[164:171], v[192:195]
	v_mfma_f32_16x16x128_f8f6f4 v[36:39], v[0:7], v[172:179], v[196:199]
	v_mfma_f32_16x16x128_f8f6f4 v[28:31], v[8:15], v[172:179], v[200:203]
	v_mfma_f32_16x16x128_f8f6f4 v[20:23], v[0:7], v[180:187], v[218:221]
	v_mfma_f32_16x16x128_f8f6f4 v[12:15], v[8:15], v[180:187], v[222:225]
	s_setprio 0
	s_setprio 1
	v_mfma_f32_16x16x128_f8f6f4 v[48:51], v[140:147], v[156:163], v[48:51]
	v_mfma_f32_16x16x128_f8f6f4 v[40:43], v[148:155], v[156:163], v[226:229]
	v_mfma_f32_16x16x128_f8f6f4 v[32:35], v[140:147], v[164:171], v[230:233]
	v_mfma_f32_16x16x128_f8f6f4 v[24:27], v[148:155], v[164:171], v[234:237]
	v_mfma_f32_16x16x128_f8f6f4 v[16:19], v[140:147], v[172:179], v[238:241]
	v_mfma_f32_16x16x128_f8f6f4 v[8:11], v[148:155], v[172:179], v[242:245]
	v_mfma_f32_16x16x128_f8f6f4 v[4:7], v[140:147], v[180:187], v[246:249]
	v_mfma_f32_16x16x128_f8f6f4 v[0:3], v[148:155], v[180:187], v[250:253]
	s_setprio 0
	s_barrier
	s_add_i32 s43, s43, 2
	s_add_u32 s41, s41, 0x100
	s_addc_u32 s42, s42, 0
	s_add_u32 s18, s18, 0x100
	s_addc_u32 s19, s19, 0
	s_cmp_gt_u32 s43, 41
	s_cbranch_scc1 .Lmy_peel2205_exit

.LBB0_2225:
	s_cmp_lt_i32 s79, 1
	s_cbranch_scc1 .LBB0_2236
	s_add_i32 s80, s79, -2
	s_add_u32 s81, s20, 0x100
	s_addc_u32 s82, s21, 0
	s_add_u32 s18, s18, 0xb0080
	s_addc_u32 s19, s19, 0
	s_mov_b32 s20, 0
	s_add_i32 s83, s20, 2
	s_add_u32 s22, s18, 0xfff50080
	s_addc_u32 s21, s19, -1
	s_add_i32 s84, 0, 0x10000
	s_cmp_eq_u32 s80, s20
	s_cselect_b32 s21, s15, s21
	s_cselect_b32 s20, s14, s22
	v_add_u32_e32 v96, s84, v145
	s_cselect_b32 s23, s17, s82
	s_cselect_b32 s22, s16, s81
	s_add_i32 s86, 0, 0x14000
	ds_read_b128 v[148:151], v96
	ds_read_b128 v[152:155], v96 offset:1024
	ds_read_b128 v[156:159], v96 offset:2048
	ds_read_b128 v[160:163], v96 offset:3072
	v_add_u32_e32 v96, s86, v145
	ds_read_b128 v[164:167], v96
	ds_read_b128 v[168:171], v96 offset:1024
	ds_read_b128 v[172:175], v96 offset:2048
	ds_read_b128 v[176:179], v96 offset:3072
	v_mov_b32_e32 v96, v138
	ds_read_b128 v[180:183], v147
	ds_read_b128 v[184:187], v147 offset:1024
	ds_read_b128 v[188:191], v147 offset:2048
	ds_read_b128 v[192:195], v147 offset:3072
	ds_read_b128 v[196:199], v147 offset:4096
	ds_read_b128 v[200:203], v147 offset:5120
	ds_read_b128 v[222:225], v147 offset:6144
	ds_read_b128 v[226:229], v147 offset:7168
	s_add_i32 m0, s26, 0xc000
	s_nop 0
	global_load_lds_dwordx4 v96, s[18:19]
	v_mov_b32_e32 v96, v140
	s_add_i32 m0, s26, 0xe000
	s_nop 0
	global_load_lds_dwordx4 v96, s[18:19]
	s_waitcnt vmcnt(8)
	s_waitcnt lgkmcnt(0)
	s_barrier
	s_setprio 1
	s_waitcnt lgkmcnt(0)
	v_mfma_f32_16x16x128_f8f6f4 v[126:129], v[148:155], v[188:195], 0
	v_mfma_f32_16x16x128_f8f6f4 v[110:113], v[156:163], v[188:195], 0
	v_mfma_f32_16x16x128_f8f6f4 v[130:133], v[148:155], v[196:203], 0
	v_mfma_f32_16x16x128_f8f6f4 v[114:117], v[156:163], v[196:203], 0
	v_mfma_f32_16x16x128_f8f6f4 v[134:137], v[148:155], v[222:229], 0
	v_mfma_f32_16x16x128_f8f6f4 v[118:121], v[156:163], v[222:229], 0
	v_mfma_f32_16x16x128_f8f6f4 v[106:109], v[148:155], v[180:187], 0
	v_mfma_f32_16x16x128_f8f6f4 v[122:125], v[156:163], v[180:187], 0
	s_setprio 0
	s_setprio 1
	v_mfma_f32_16x16x128_f8f6f4 v[92:95], v[164:171], v[180:187], 0
	v_mfma_f32_16x16x128_f8f6f4 v[68:71], v[172:179], v[180:187], 0
	v_mfma_f32_16x16x128_f8f6f4 v[180:183], v[164:171], v[188:195], 0
	v_mfma_f32_16x16x128_f8f6f4 v[184:187], v[172:179], v[188:195], 0
	v_mfma_f32_16x16x128_f8f6f4 v[188:191], v[164:171], v[196:203], 0
	v_mfma_f32_16x16x128_f8f6f4 v[192:195], v[172:179], v[196:203], 0
	v_mfma_f32_16x16x128_f8f6f4 v[196:199], v[164:171], v[222:229], 0
	v_mfma_f32_16x16x128_f8f6f4 v[200:203], v[172:179], v[222:229], 0
	s_setprio 0
	s_barrier
	v_mov_b32_e32 v96, v139
	s_add_i32 s84, s84, s25
	s_nop 2
	ds_read_b128 v[60:63], v147 offset:16384
	ds_read_b128 v[64:67], v147 offset:17408
	ds_read_b128 v[76:79], v147 offset:18432
	ds_read_b128 v[80:83], v147 offset:19456
	ds_read_b128 v[84:87], v147 offset:20480
	ds_read_b128 v[88:91], v147 offset:21504
	ds_read_b128 v[98:101], v147 offset:22528
	ds_read_b128 v[102:105], v147 offset:23552
	s_mov_b32 m0, s84
	s_nop 0
	global_load_lds_dwordx4 v96, s[22:23]
	v_mov_b32_e32 v96, v141
	s_add_i32 m0, s84, 0x2000
	s_add_u32 s84, s22, 0xb0000
	global_load_lds_dwordx4 v96, s[22:23]
	s_addc_u32 s85, s23, 0
	v_mov_b32_e32 v96, v139
	s_add_i32 s86, s86, s25
	s_mov_b32 m0, s86
	s_nop 0
	global_load_lds_dwordx4 v96, s[84:85]
	v_mov_b32_e32 v96, v141
	s_add_i32 m0, s86, 0x2000
	s_nop 0
	global_load_lds_dwordx4 v96, s[84:85]
	v_mov_b32_e32 v96, v138
	s_mov_b32 m0, s26
	s_nop 0
	global_load_lds_dwordx4 v96, s[20:21]
	v_mov_b32_e32 v96, v140
	s_mov_b32 m0, s27
	s_nop 0
	global_load_lds_dwordx4 v96, s[20:21]
	s_waitcnt vmcnt(8)
	s_waitcnt lgkmcnt(0)
	s_barrier
	s_setprio 1
	s_waitcnt lgkmcnt(0)
	v_mfma_f32_16x16x128_f8f6f4 v[72:75], v[148:155], v[60:67], 0
	v_mfma_f32_16x16x128_f8f6f4 v[56:59], v[156:163], v[60:67], 0
	v_mfma_f32_16x16x128_f8f6f4 v[52:55], v[148:155], v[76:83], 0
	v_mfma_f32_16x16x128_f8f6f4 v[48:51], v[156:163], v[76:83], 0
	v_mfma_f32_16x16x128_f8f6f4 v[204:207], v[148:155], v[84:91], 0
	v_mfma_f32_16x16x128_f8f6f4 v[208:211], v[156:163], v[84:91], 0
	v_mfma_f32_16x16x128_f8f6f4 v[212:215], v[148:155], v[98:105], 0
	v_mfma_f32_16x16x128_f8f6f4 v[218:221], v[156:163], v[98:105], 0
	s_setprio 0
	s_setprio 1
	v_mfma_f32_16x16x128_f8f6f4 v[222:225], v[164:171], v[60:67], 0
	v_mfma_f32_16x16x128_f8f6f4 v[226:229], v[172:179], v[60:67], 0
	v_mfma_f32_16x16x128_f8f6f4 v[230:233], v[164:171], v[76:83], 0
	v_mfma_f32_16x16x128_f8f6f4 v[234:237], v[172:179], v[76:83], 0
	v_mfma_f32_16x16x128_f8f6f4 v[238:241], v[164:171], v[84:91], 0
	v_mfma_f32_16x16x128_f8f6f4 v[242:245], v[172:179], v[84:91], 0
	v_mfma_f32_16x16x128_f8f6f4 v[246:249], v[164:171], v[98:105], 0
	v_mfma_f32_16x16x128_f8f6f4 v[250:253], v[172:179], v[98:105], 0
	s_setprio 0
	s_barrier
	s_add_i32 s86, 0, 0x18000
	s_add_i32 s87, 0, 0x1c000
	v_add_u32_e32 v12, s86, v145
	v_add_u32_e32 v16, s87, v145
	s_nop 0
	ds_read_b128 v[0:3], v12
	ds_read_b128 v[4:7], v12 offset:1024
	ds_read_b128 v[8:11], v12 offset:2048
	ds_read_b128 v[12:15], v12 offset:3072
	ds_read_b128 v[148:151], v16
	ds_read_b128 v[152:155], v16 offset:1024
	ds_read_b128 v[156:159], v16 offset:2048
	ds_read_b128 v[160:163], v16 offset:3072
	s_add_u32 s84, s20, 0xb0000
	v_mov_b32_e32 v60, v138
	s_mov_b32 m0, s28
	ds_read_b128 v[16:19], v147 offset:32768
	ds_read_b128 v[20:23], v147 offset:33792
	ds_read_b128 v[24:27], v147 offset:34816
	ds_read_b128 v[28:31], v147 offset:35840
	ds_read_b128 v[32:35], v147 offset:36864
	ds_read_b128 v[36:39], v147 offset:37888
	ds_read_b128 v[40:43], v147 offset:38912
	ds_read_b128 v[44:47], v147 offset:39936
	s_addc_u32 s85, s21, 0
	s_nop 0
	global_load_lds_dwordx4 v60, s[84:85]
	v_mov_b32_e32 v60, v140
	s_mov_b32 m0, s29
	s_nop 0
	global_load_lds_dwordx4 v60, s[84:85]
	s_waitcnt vmcnt(8)
	s_waitcnt lgkmcnt(0)
	s_barrier
	s_setprio 1
	s_waitcnt lgkmcnt(0)
	v_mfma_f32_16x16x128_f8f6f4 v[64:67], v[0:7], v[16:23], v[106:109]
	v_mfma_f32_16x16x128_f8f6f4 v[88:91], v[8:15], v[16:23], v[122:125]
	v_mfma_f32_16x16x128_f8f6f4 v[126:129], v[0:7], v[24:31], v[126:129]
	v_mfma_f32_16x16x128_f8f6f4 v[110:113], v[8:15], v[24:31], v[110:113]
	v_mfma_f32_16x16x128_f8f6f4 v[130:133], v[0:7], v[32:39], v[130:133]
	v_mfma_f32_16x16x128_f8f6f4 v[114:117], v[8:15], v[32:39], v[114:117]
	v_mfma_f32_16x16x128_f8f6f4 v[134:137], v[0:7], v[40:47], v[134:137]
	v_mfma_f32_16x16x128_f8f6f4 v[118:121], v[8:15], v[40:47], v[118:121]
	s_setprio 0
	s_setprio 1
	v_mfma_f32_16x16x128_f8f6f4 v[92:95], v[148:155], v[16:23], v[92:95]
	v_mfma_f32_16x16x128_f8f6f4 v[68:71], v[156:163], v[16:23], v[68:71]
	v_mfma_f32_16x16x128_f8f6f4 v[98:101], v[148:155], v[24:31], v[180:183]
	v_mfma_f32_16x16x128_f8f6f4 v[80:83], v[156:163], v[24:31], v[184:187]
	v_mfma_f32_16x16x128_f8f6f4 v[102:105], v[148:155], v[32:39], v[188:191]
	v_mfma_f32_16x16x128_f8f6f4 v[84:87], v[156:163], v[32:39], v[192:195]
	v_mfma_f32_16x16x128_f8f6f4 v[76:79], v[148:155], v[40:47], v[196:199]
	v_mfma_f32_16x16x128_f8f6f4 v[60:63], v[156:163], v[40:47], v[200:203]
	s_setprio 0
	s_barrier
	v_mov_b32_e32 v96, v139
	ds_read_b128 v[164:167], v147 offset:49152
	ds_read_b128 v[168:171], v147 offset:50176
	ds_read_b128 v[172:175], v147 offset:51200
	ds_read_b128 v[176:179], v147 offset:52224
	ds_read_b128 v[180:183], v147 offset:53248
	ds_read_b128 v[184:187], v147 offset:54272
	ds_read_b128 v[188:191], v147 offset:55296
	ds_read_b128 v[192:195], v147 offset:56320
	s_add_i32 s84, s86, s25
	v_lshl_add_u64 v[16:17], s[22:23], 0, v[96:97]
	v_lshl_add_u64 v[16:17], v[16:17], 0, s[0:1]
	s_mov_b32 m0, s84
	v_mov_b32_e32 v96, v141
	global_load_lds_dwordx4 v[16:17], off
	s_add_i32 m0, s84, 0x2000
	v_lshl_add_u64 v[16:17], s[22:23], 0, v[96:97]
	v_lshl_add_u64 v[16:17], v[16:17], 0, s[0:1]
	s_add_u32 s22, s22, 0xb0080
	global_load_lds_dwordx4 v[16:17], off
	s_addc_u32 s23, s23, 0
	v_mov_b32_e32 v16, v139
	s_add_i32 s84, s87, s25
	s_mov_b32 m0, s84
	v_mov_b32_e32 v96, v138
	global_load_lds_dwordx4 v16, s[22:23]
	v_mov_b32_e32 v16, v141
	s_add_i32 m0, s84, 0x2000
	s_nop 0
	global_load_lds_dwordx4 v16, s[22:23]
	s_mov_b32 m0, s35
	v_lshl_add_u64 v[16:17], s[20:21], 0, v[96:97]
	v_lshl_add_u64 v[16:17], v[16:17], 0, s[0:1]
	v_mov_b32_e32 v96, v140
	global_load_lds_dwordx4 v[16:17], off
	s_mov_b32 m0, s36
	v_lshl_add_u64 v[16:17], s[20:21], 0, v[96:97]
	v_lshl_add_u64 v[16:17], v[16:17], 0, s[0:1]
	global_load_lds_dwordx4 v[16:17], off
	s_waitcnt vmcnt(8)
	s_waitcnt lgkmcnt(0)
	s_barrier
	s_setprio 1
	s_waitcnt lgkmcnt(0)
	v_mfma_f32_16x16x128_f8f6f4 v[72:75], v[0:7], v[164:171], v[72:75]
	v_mfma_f32_16x16x128_f8f6f4 v[56:59], v[8:15], v[164:171], v[56:59]
	v_mfma_f32_16x16x128_f8f6f4 v[52:55], v[0:7], v[172:179], v[52:55]
	v_mfma_f32_16x16x128_f8f6f4 v[48:51], v[8:15], v[172:179], v[48:51]
	v_mfma_f32_16x16x128_f8f6f4 v[40:43], v[0:7], v[180:187], v[204:207]
	v_mfma_f32_16x16x128_f8f6f4 v[32:35], v[8:15], v[180:187], v[208:211]
	v_mfma_f32_16x16x128_f8f6f4 v[24:27], v[0:7], v[188:195], v[212:215]
	v_mfma_f32_16x16x128_f8f6f4 v[16:19], v[8:15], v[188:195], v[218:221]
	s_setprio 0
	s_setprio 1
	v_mfma_f32_16x16x128_f8f6f4 v[44:47], v[148:155], v[164:171], v[222:225]
	v_mfma_f32_16x16x128_f8f6f4 v[36:39], v[156:163], v[164:171], v[226:229]
	v_mfma_f32_16x16x128_f8f6f4 v[28:31], v[148:155], v[172:179], v[230:233]
	v_mfma_f32_16x16x128_f8f6f4 v[20:23], v[156:163], v[172:179], v[234:237]
	v_mfma_f32_16x16x128_f8f6f4 v[12:15], v[148:155], v[180:187], v[238:241]
	v_mfma_f32_16x16x128_f8f6f4 v[8:11], v[156:163], v[180:187], v[242:245]
	v_mfma_f32_16x16x128_f8f6f4 v[4:7], v[148:155], v[188:195], v[246:249]
	v_mfma_f32_16x16x128_f8f6f4 v[0:3], v[156:163], v[188:195], v[250:253]
	s_setprio 0
	s_barrier
	s_add_u32 s81, s81, 0x100
	s_addc_u32 s82, s82, 0
	s_add_u32 s18, s18, 0x100
	s_addc_u32 s19, s19, 0
	s_cmp_ge_i32 s83, s79
	s_mov_b32 s20, s83
	s_cbranch_scc1 .Lmy_peel2227_exit

.Lmy_peel2227_exit:
	v_pk_mul_f32 v[66:67], v[66:67], s[58:59] op_sel_hi:[1,0]
	v_pk_mul_f32 v[64:65], v[64:65], s[58:59] op_sel_hi:[1,0]
	v_pk_mul_f32 v[90:91], v[90:91], s[58:59] op_sel_hi:[1,0]
	v_pk_mul_f32 v[88:89], v[88:89], s[58:59] op_sel_hi:[1,0]
	v_pk_mul_f32 v[108:109], v[94:95], s[58:59] op_sel_hi:[1,0]
	v_pk_mul_f32 v[106:107], v[92:93], s[58:59] op_sel_hi:[1,0]
	v_pk_mul_f32 v[124:125], v[70:71], s[58:59] op_sel_hi:[1,0]
	v_pk_mul_f32 v[122:123], v[68:69], s[58:59] op_sel_hi:[1,0]
	v_pk_mul_f32 v[70:71], v[128:129], s[58:59] op_sel_hi:[1,0]
	v_pk_mul_f32 v[68:69], v[126:127], s[58:59] op_sel_hi:[1,0]
	v_pk_mul_f32 v[94:95], v[112:113], s[58:59] op_sel_hi:[1,0]
	v_pk_mul_f32 v[92:93], v[110:111], s[58:59] op_sel_hi:[1,0]
	v_pk_mul_f32 v[112:113], v[100:101], s[58:59] op_sel_hi:[1,0]
	v_pk_mul_f32 v[110:111], v[98:99], s[58:59] op_sel_hi:[1,0]
	v_pk_mul_f32 v[128:129], v[82:83], s[58:59] op_sel_hi:[1,0]
	v_pk_mul_f32 v[126:127], v[80:81], s[58:59] op_sel_hi:[1,0]
	v_pk_mul_f32 v[82:83], v[132:133], s[58:59] op_sel_hi:[1,0]
	v_pk_mul_f32 v[80:81], v[130:131], s[58:59] op_sel_hi:[1,0]
	v_pk_mul_f32 v[100:101], v[116:117], s[58:59] op_sel_hi:[1,0]
	v_pk_mul_f32 v[98:99], v[114:115], s[58:59] op_sel_hi:[1,0]
	v_pk_mul_f32 v[116:117], v[104:105], s[58:59] op_sel_hi:[1,0]
	v_pk_mul_f32 v[114:115], v[102:103], s[58:59] op_sel_hi:[1,0]
	v_pk_mul_f32 v[132:133], v[86:87], s[58:59] op_sel_hi:[1,0]
	v_pk_mul_f32 v[130:131], v[84:85], s[58:59] op_sel_hi:[1,0]
	v_pk_mul_f32 v[86:87], v[136:137], s[58:59] op_sel_hi:[1,0]
	v_pk_mul_f32 v[84:85], v[134:135], s[58:59] op_sel_hi:[1,0]
	v_pk_mul_f32 v[104:105], v[120:121], s[58:59] op_sel_hi:[1,0]
	v_pk_mul_f32 v[102:103], v[118:119], s[58:59] op_sel_hi:[1,0]
	v_pk_mul_f32 v[78:79], v[78:79], s[58:59] op_sel_hi:[1,0]
	v_pk_mul_f32 v[76:77], v[76:77], s[58:59] op_sel_hi:[1,0]
	v_pk_mul_f32 v[120:121], v[62:63], s[58:59] op_sel_hi:[1,0]
	v_pk_mul_f32 v[118:119], v[60:61], s[58:59] op_sel_hi:[1,0]
	v_pk_mul_f32 v[62:63], v[74:75], s[58:59] op_sel_hi:[1,0]
	v_pk_mul_f32 v[60:61], v[72:73], s[58:59] op_sel_hi:[1,0]
	v_pk_mul_f32 v[58:59], v[58:59], s[58:59] op_sel_hi:[1,0]
	v_pk_mul_f32 v[56:57], v[56:57], s[58:59] op_sel_hi:[1,0]
	v_pk_mul_f32 v[74:75], v[46:47], s[58:59] op_sel_hi:[1,0]
	v_pk_mul_f32 v[72:73], v[44:45], s[58:59] op_sel_hi:[1,0]
	v_pk_mul_f32 v[136:137], v[38:39], s[58:59] op_sel_hi:[1,0]
	v_pk_mul_f32 v[134:135], v[36:37], s[58:59] op_sel_hi:[1,0]
	v_pk_mul_f32 v[38:39], v[54:55], s[58:59] op_sel_hi:[1,0]
	v_pk_mul_f32 v[36:37], v[52:53], s[58:59] op_sel_hi:[1,0]
	v_pk_mul_f32 v[46:47], v[50:51], s[58:59] op_sel_hi:[1,0]
	v_pk_mul_f32 v[44:45], v[48:49], s[58:59] op_sel_hi:[1,0]
	v_pk_mul_f32 v[50:51], v[30:31], s[58:59] op_sel_hi:[1,0]
	v_pk_mul_f32 v[48:49], v[28:29], s[58:59] op_sel_hi:[1,0]
	v_pk_mul_f32 v[54:55], v[22:23], s[58:59] op_sel_hi:[1,0]
	v_pk_mul_f32 v[52:53], v[20:21], s[58:59] op_sel_hi:[1,0]
	v_pk_mul_f32 v[22:23], v[42:43], s[58:59] op_sel_hi:[1,0]
	v_pk_mul_f32 v[20:21], v[40:41], s[58:59] op_sel_hi:[1,0]
	v_pk_mul_f32 v[30:31], v[34:35], s[58:59] op_sel_hi:[1,0]
	v_pk_mul_f32 v[28:29], v[32:33], s[58:59] op_sel_hi:[1,0]
	v_pk_mul_f32 v[34:35], v[14:15], s[58:59] op_sel_hi:[1,0]
	v_pk_mul_f32 v[32:33], v[12:13], s[58:59] op_sel_hi:[1,0]
	v_pk_mul_f32 v[42:43], v[10:11], s[58:59] op_sel_hi:[1,0]
	v_pk_mul_f32 v[40:41], v[8:9], s[58:59] op_sel_hi:[1,0]
	v_pk_mul_f32 v[10:11], v[26:27], s[58:59] op_sel_hi:[1,0]
	v_pk_mul_f32 v[8:9], v[24:25], s[58:59] op_sel_hi:[1,0]
	v_pk_mul_f32 v[14:15], v[18:19], s[58:59] op_sel_hi:[1,0]
	v_pk_mul_f32 v[12:13], v[16:17], s[58:59] op_sel_hi:[1,0]
	v_pk_mul_f32 v[6:7], v[6:7], s[58:59] op_sel_hi:[1,0]
	v_pk_mul_f32 v[4:5], v[4:5], s[58:59] op_sel_hi:[1,0]
	v_pk_mul_f32 v[2:3], v[2:3], s[58:59] op_sel_hi:[1,0]
	v_pk_mul_f32 v[0:1], v[0:1], s[58:59] op_sel_hi:[1,0]
	s_and_b64 vcc, exec, s[8:9]
	s_cbranch_vccz .LBB0_2230
